# RG-LRU conv: tap weights stored pair-transposed in LDS so the packed FMAs read aligned weight pairs directly (48 register shuffles per tile removed)
# baseline (speedup 1.0000x reference)
; #define LAS __attribute__((address_space(3)))
; __device__ __forceinline__ unsigned pk2(float lo, float hi) { const pk2_f32x2 v = {lo, hi}; return __builtin_bit_cast(unsigned, __builtin_convertvector(v, pk2_bf16x2)); }
; __device__ __forceinline__ void rec1_unit(KArgs args, int L, int unit, LAS unsigned char* lds, int wave, int lane) {
;     ...
;     for (int f = 0; f < 16; ++f) { const int mat = f >> 3, n = (f >> 1) & 3, kk = f & 1; const float* W = mat ? Wx : Wa;
;         const int jout = 8 * (fr >> 2) + (fr & 3) + 4 * (n & 1) + 32 * (n >> 1); const float* wp = W + (32 * kk + 8 * q) * 64 + jout;
;         u32x4 w; w.x = pk2(wp[0], wp[64]); w.y = pk2(wp[128], wp[192]); w.z = pk2(wp[256], wp[320]); w.w = pk2(wp[384], wp[448]);
;         *(LAS u32x4*)(wl + f * 1024 + lane * 16) = w; }
.LBB0_175:
	v_add_lshl_u32 v4, v145, v144, 2
	v_mov_b32_e32 v5, v0
	s_add_u32 s14, s8, s16
	s_addc_u32 s15, s9, s17
	s_add_u32 s0, s14, 0x2000
	s_addc_u32 s1, s15, 0
	v_lshl_add_u64 v[6:7], s[14:15], 0, v[4:5]
	v_lshl_add_u64 v[8:9], s[0:1], 0, v[4:5]
	global_load_dword v10, v[6:7], off
	global_load_dword v11, v[6:7], off offset:256
	global_load_dword v12, v[6:7], off offset:512
	global_load_dword v13, v[6:7], off offset:768
	global_load_dword v14, v[6:7], off offset:1024
	global_load_dword v15, v[6:7], off offset:1280
	global_load_dword v16, v[6:7], off offset:1536
	global_load_dword v17, v[6:7], off offset:1792
	global_load_dword v18, v[8:9], off
	global_load_dword v19, v[8:9], off offset:256
	global_load_dword v20, v[8:9], off offset:512
	global_load_dword v21, v[8:9], off offset:768
	global_load_dword v22, v[8:9], off offset:1024
	global_load_dword v23, v[8:9], off offset:1280
	global_load_dword v24, v[8:9], off offset:1536
	global_load_dword v25, v[8:9], off offset:1792
	global_load_dword v26, v[6:7], off offset:16
	global_load_dword v27, v[6:7], off offset:272
	global_load_dword v28, v[6:7], off offset:528
	global_load_dword v29, v[6:7], off offset:784
	global_load_dword v30, v[6:7], off offset:1040
	global_load_dword v31, v[6:7], off offset:1296
	global_load_dword v32, v[6:7], off offset:1552
	global_load_dword v33, v[6:7], off offset:1808
	global_load_dword v34, v[8:9], off offset:16
	global_load_dword v35, v[8:9], off offset:272
	global_load_dword v36, v[8:9], off offset:528
	global_load_dword v37, v[8:9], off offset:784
	global_load_dword v38, v[8:9], off offset:1040
	global_load_dword v39, v[8:9], off offset:1296
	global_load_dword v40, v[8:9], off offset:1552
	global_load_dword v41, v[8:9], off offset:1808
	global_load_dword v42, v[6:7], off offset:128
	global_load_dword v43, v[6:7], off offset:384
	global_load_dword v44, v[6:7], off offset:640
	global_load_dword v45, v[6:7], off offset:896
	global_load_dword v46, v[6:7], off offset:1152
	global_load_dword v47, v[6:7], off offset:1408
	global_load_dword v48, v[6:7], off offset:1664
	global_load_dword v49, v[6:7], off offset:1920
	global_load_dword v50, v[8:9], off offset:128
	global_load_dword v51, v[8:9], off offset:384
	global_load_dword v52, v[8:9], off offset:640
	global_load_dword v53, v[8:9], off offset:896
	global_load_dword v54, v[8:9], off offset:1152
	global_load_dword v55, v[8:9], off offset:1408
	global_load_dword v56, v[8:9], off offset:1664
	global_load_dword v57, v[8:9], off offset:1920
	global_load_dword v58, v[6:7], off offset:144
	global_load_dword v59, v[6:7], off offset:400
	global_load_dword v60, v[6:7], off offset:656
	global_load_dword v61, v[6:7], off offset:912
	global_load_dword v62, v[6:7], off offset:1168
	global_load_dword v63, v[6:7], off offset:1424
	global_load_dword v64, v[6:7], off offset:1680
	global_load_dword v65, v[6:7], off offset:1936
	global_load_dword v66, v[8:9], off offset:144
	global_load_dword v67, v[8:9], off offset:400
	global_load_dword v68, v[8:9], off offset:656
	global_load_dword v69, v[8:9], off offset:912
	global_load_dword v70, v[8:9], off offset:1168
	global_load_dword v71, v[8:9], off offset:1424
	global_load_dword v72, v[8:9], off offset:1680
	global_load_dword v73, v[8:9], off offset:1936
	s_waitcnt vmcnt(0)
	v_cvt_pk_bf16_f32 v10, v10, v11
	v_cvt_pk_bf16_f32 v11, v12, v13
	v_cvt_pk_bf16_f32 v12, v14, v15
	v_cvt_pk_bf16_f32 v13, v16, v17
	ds_write_b128 v146, v[10:13]
	v_cvt_pk_bf16_f32 v18, v18, v19
	v_cvt_pk_bf16_f32 v19, v20, v21
	v_cvt_pk_bf16_f32 v20, v22, v23
	v_cvt_pk_bf16_f32 v21, v24, v25
	ds_write_b128 v146, v[18:21] offset:1024
	v_cvt_pk_bf16_f32 v26, v26, v27
	v_cvt_pk_bf16_f32 v27, v28, v29
	v_cvt_pk_bf16_f32 v28, v30, v31
	v_cvt_pk_bf16_f32 v29, v32, v33
	ds_write_b128 v146, v[26:29] offset:2048
	v_cvt_pk_bf16_f32 v34, v34, v35
	v_cvt_pk_bf16_f32 v35, v36, v37
	v_cvt_pk_bf16_f32 v36, v38, v39
	v_cvt_pk_bf16_f32 v37, v40, v41
	ds_write_b128 v146, v[34:37] offset:3072
	v_cvt_pk_bf16_f32 v42, v42, v43
	v_cvt_pk_bf16_f32 v43, v44, v45
	v_cvt_pk_bf16_f32 v44, v46, v47
	v_cvt_pk_bf16_f32 v45, v48, v49
	ds_write_b128 v146, v[42:45] offset:4096
	v_cvt_pk_bf16_f32 v50, v50, v51
	v_cvt_pk_bf16_f32 v51, v52, v53
	v_cvt_pk_bf16_f32 v52, v54, v55
	v_cvt_pk_bf16_f32 v53, v56, v57
	ds_write_b128 v146, v[50:53] offset:5120
	v_cvt_pk_bf16_f32 v58, v58, v59
	v_cvt_pk_bf16_f32 v59, v60, v61
	v_cvt_pk_bf16_f32 v60, v62, v63
	v_cvt_pk_bf16_f32 v61, v64, v65
	ds_write_b128 v146, v[58:61] offset:6144
	v_cvt_pk_bf16_f32 v66, v66, v67
	v_cvt_pk_bf16_f32 v67, v68, v69
	v_cvt_pk_bf16_f32 v68, v70, v71
	v_cvt_pk_bf16_f32 v69, v72, v73
	ds_write_b128 v146, v[66:69] offset:7168
	s_add_u32 s14, s12, s16
	s_addc_u32 s15, s13, s17
	s_add_u32 s0, s14, 0x2000
	s_addc_u32 s1, s15, 0
	v_lshl_add_u64 v[6:7], s[14:15], 0, v[4:5]
	v_lshl_add_u64 v[8:9], s[0:1], 0, v[4:5]
	s_waitcnt lgkmcnt(0)
; #define LAS __attribute__((address_space(3)))
; #define LDS_WAIT() asm volatile("s_waitcnt lgkmcnt(0)" ::: "memory")
; __device__ __forceinline__ unsigned pk2(float lo, float hi) { const pk2_f32x2 v = {lo, hi}; return __builtin_bit_cast(unsigned, __builtin_convertvector(v, pk2_bf16x2)); }
; __device__ __forceinline__ void rec1_unit(KArgs args, int L, int unit, LAS unsigned char* lds, int wave, int lane) {
;     ...
;     for (int f = 0; f < 16; ++f) { const int mat = f >> 3, n = (f >> 1) & 3, kk = f & 1; const float* W = mat ? Wx : Wa;
;         const int jout = 8 * (fr >> 2) + (fr & 3) + 4 * (n & 1) + 32 * (n >> 1); const float* wp = W + (32 * kk + 8 * q) * 64 + jout;
;         u32x4 w; w.x = pk2(wp[0], wp[64]); w.y = pk2(wp[128], wp[192]); w.z = pk2(wp[256], wp[320]); w.w = pk2(wp[384], wp[448]);
;         *(LAS u32x4*)(wl + f * 1024 + lane * 16) = w; }
;     LAS float* ct = (LAS float*)(lds + 131072 + wave * 2048);
;     { const int c = 64 * hb + lane; const float* cw = args->in[I_CONVW] + (size_t)L * 4 * 512;
;       ct[lane * 8 + 0] = cw[c]; ct[lane * 8 + 1] = cw[512 + c]; ct[lane * 8 + 2] = cw[1024 + c]; ct[lane * 8 + 3] = cw[1536 + c];
;       ct[lane * 8 + 4] = args->in[I_CONVB][L * 512 + c]; ct[lane * 8 + 5] = args->in[I_BA][L * 512 + c]; ct[lane * 8 + 6] = args->in[I_BX][L * 512 + c];
;       ct[lane * 8 + 7] = ((const float*)(ws + WS_C8))[L * 512 + c]; }
;     LDS_WAIT();
	global_load_dword v10, v[6:7], off
	global_load_dword v11, v[6:7], off offset:256
	global_load_dword v12, v[6:7], off offset:512
	global_load_dword v13, v[6:7], off offset:768
	global_load_dword v14, v[6:7], off offset:1024
	global_load_dword v15, v[6:7], off offset:1280
	global_load_dword v16, v[6:7], off offset:1536
	global_load_dword v17, v[6:7], off offset:1792
	global_load_dword v18, v[8:9], off
	global_load_dword v19, v[8:9], off offset:256
	global_load_dword v20, v[8:9], off offset:512
	global_load_dword v21, v[8:9], off offset:768
	global_load_dword v22, v[8:9], off offset:1024
	global_load_dword v23, v[8:9], off offset:1280
	global_load_dword v24, v[8:9], off offset:1536
	global_load_dword v25, v[8:9], off offset:1792
	global_load_dword v26, v[6:7], off offset:16
	global_load_dword v27, v[6:7], off offset:272
	global_load_dword v28, v[6:7], off offset:528
	global_load_dword v29, v[6:7], off offset:784
	global_load_dword v30, v[6:7], off offset:1040
	global_load_dword v31, v[6:7], off offset:1296
	global_load_dword v32, v[6:7], off offset:1552
	global_load_dword v33, v[6:7], off offset:1808
	global_load_dword v34, v[8:9], off offset:16
	global_load_dword v35, v[8:9], off offset:272
	global_load_dword v36, v[8:9], off offset:528
	global_load_dword v37, v[8:9], off offset:784
	global_load_dword v38, v[8:9], off offset:1040
	global_load_dword v39, v[8:9], off offset:1296
	global_load_dword v40, v[8:9], off offset:1552
	global_load_dword v41, v[8:9], off offset:1808
	global_load_dword v42, v[6:7], off offset:128
	global_load_dword v43, v[6:7], off offset:384
	global_load_dword v44, v[6:7], off offset:640
	global_load_dword v45, v[6:7], off offset:896
	global_load_dword v46, v[6:7], off offset:1152
	global_load_dword v47, v[6:7], off offset:1408
	global_load_dword v48, v[6:7], off offset:1664
	global_load_dword v49, v[6:7], off offset:1920
	global_load_dword v50, v[8:9], off offset:128
	global_load_dword v51, v[8:9], off offset:384
	global_load_dword v52, v[8:9], off offset:640
	global_load_dword v53, v[8:9], off offset:896
	global_load_dword v54, v[8:9], off offset:1152
	global_load_dword v55, v[8:9], off offset:1408
	global_load_dword v56, v[8:9], off offset:1664
	global_load_dword v57, v[8:9], off offset:1920
	global_load_dword v58, v[6:7], off offset:144
	global_load_dword v59, v[6:7], off offset:400
	global_load_dword v60, v[6:7], off offset:656
	global_load_dword v61, v[6:7], off offset:912
	global_load_dword v62, v[6:7], off offset:1168
	global_load_dword v63, v[6:7], off offset:1424
	global_load_dword v64, v[6:7], off offset:1680
	global_load_dword v65, v[6:7], off offset:1936
	global_load_dword v66, v[8:9], off offset:144
	global_load_dword v67, v[8:9], off offset:400
	global_load_dword v68, v[8:9], off offset:656
	global_load_dword v69, v[8:9], off offset:912
	global_load_dword v70, v[8:9], off offset:1168
	global_load_dword v71, v[8:9], off offset:1424
	global_load_dword v72, v[8:9], off offset:1680
	global_load_dword v73, v[8:9], off offset:1936
	s_waitcnt vmcnt(0)
	v_cvt_pk_bf16_f32 v10, v10, v11
	v_cvt_pk_bf16_f32 v11, v12, v13
	v_cvt_pk_bf16_f32 v12, v14, v15
	v_cvt_pk_bf16_f32 v13, v16, v17
	ds_write_b128 v146, v[10:13] offset:8192
	v_cvt_pk_bf16_f32 v18, v18, v19
	v_cvt_pk_bf16_f32 v19, v20, v21
	v_cvt_pk_bf16_f32 v20, v22, v23
	v_cvt_pk_bf16_f32 v21, v24, v25
	ds_write_b128 v146, v[18:21] offset:9216
	v_cvt_pk_bf16_f32 v26, v26, v27
	v_cvt_pk_bf16_f32 v27, v28, v29
	v_cvt_pk_bf16_f32 v28, v30, v31
	v_cvt_pk_bf16_f32 v29, v32, v33
	ds_write_b128 v146, v[26:29] offset:10240
	v_cvt_pk_bf16_f32 v34, v34, v35
	v_cvt_pk_bf16_f32 v35, v36, v37
	v_cvt_pk_bf16_f32 v36, v38, v39
	v_cvt_pk_bf16_f32 v37, v40, v41
	ds_write_b128 v146, v[34:37] offset:11264
	v_cvt_pk_bf16_f32 v42, v42, v43
	v_cvt_pk_bf16_f32 v43, v44, v45
	v_cvt_pk_bf16_f32 v44, v46, v47
	v_cvt_pk_bf16_f32 v45, v48, v49
	ds_write_b128 v146, v[42:45] offset:12288
	v_cvt_pk_bf16_f32 v50, v50, v51
	v_cvt_pk_bf16_f32 v51, v52, v53
	v_cvt_pk_bf16_f32 v52, v54, v55
	v_cvt_pk_bf16_f32 v53, v56, v57
	ds_write_b128 v146, v[50:53] offset:13312
	v_cvt_pk_bf16_f32 v58, v58, v59
	v_cvt_pk_bf16_f32 v59, v60, v61
	v_cvt_pk_bf16_f32 v60, v62, v63
	v_cvt_pk_bf16_f32 v61, v64, v65
	ds_write_b128 v146, v[58:61] offset:14336
	v_cvt_pk_bf16_f32 v66, v66, v67
	v_cvt_pk_bf16_f32 v67, v68, v69
	v_cvt_pk_bf16_f32 v68, v70, v71
	v_cvt_pk_bf16_f32 v69, v72, v73
	ds_write_b128 v146, v[66:69] offset:15360
	global_load_dword v4, v[100:101], off
	global_load_dword v5, v[100:101], off offset:2048
	global_load_dword v6, v[102:103], off
	global_load_dword v7, v[104:105], off
	global_load_dword v8, v[106:107], off
	global_load_dword v9, v[108:109], off
	global_load_dword v10, v[110:111], off
	global_load_dword v11, v[112:113], off
	s_lshl_b32 s0, s10, 8
	s_and_b32 s4, s0, 0xf00
	s_and_b32 s0, s0, 0xfffff000
	v_add_u32_e32 v152, s4, v148
	v_mad_i64_i32 v[2:3], s[0:1], s0, v209, v[114:115]
	v_or_b32_e32 v12, s4, v147
	v_max_i32_e32 v14, 0, v152
	v_max_i32_e32 v16, -1, v152
	v_max_i32_e32 v17, -2, v152
	v_mov_b32_e32 v13, v0
	v_mul_u32_u24_e32 v12, 0x1400, v12
	v_mad_u64_u32 v[14:15], s[0:1], v14, s88, v[2:3]
	v_add_u32_e32 v16, 1, v16
	v_add_u32_e32 v18, 2, v17
	v_lshl_add_u64 v[12:13], v[2:3], 0, v[12:13]
	v_mad_u64_u32 v[16:17], s[0:1], v16, s88, v[2:3]
	v_mad_u64_u32 v[18:19], s[0:1], v18, s88, v[2:3]
	s_and_b32 s11, s27, 0xf00
	s_and_b32 s0, s27, 0xfffff000
	v_or_b32_e32 v153, s11, v147
	s_waitcnt lgkmcnt(3)
; #define LDS_WAIT() asm volatile("s_waitcnt lgkmcnt(0)" ::: "memory")
; __device__ __forceinline__ unsigned pk2(float lo, float hi) { const pk2_f32x2 v = {lo, hi}; return __builtin_bit_cast(unsigned, __builtin_convertvector(v, pk2_bf16x2)); }
; __device__ __forceinline__ void rec1_unit(KArgs args, int L, int unit, LAS unsigned char* lds, int wave, int lane) {
;     ...
;     { const int c = 64 * hb + lane; const float* cw = args->in[I_CONVW] + (size_t)L * 4 * 512;
;       ct[lane * 8 + 0] = cw[c]; ct[lane * 8 + 1] = cw[512 + c]; ct[lane * 8 + 2] = cw[1024 + c]; ct[lane * 8 + 3] = cw[1536 + c];
;       ct[lane * 8 + 4] = args->in[I_CONVB][L * 512 + c]; ct[lane * 8 + 5] = args->in[I_BA][L * 512 + c]; ct[lane * 8 + 6] = args->in[I_BX][L * 512 + c];
;       ct[lane * 8 + 7] = ((const float*)(ws + WS_C8))[L * 512 + c]; }
;     LDS_WAIT();
;     ...
;             for (int e = 0; e < 8; ++e) xc[e] = ct[(32 * kk + 8 * q + e) * 8 + 4];
; #pragma unroll
;             for (int j = 0; j < 4; ++j) { const int tt = t - 3 + j;
;                 u32x4 raw = rawc[kk][j];
;                 if (edge && tt < 0) raw = (u32x4){0u, 0u, 0u, 0u};
;                 const float xv[8] = {bflo(raw.x), bfhi(raw.x), bflo(raw.y), bfhi(raw.y), bflo(raw.z), bfhi(raw.z), bflo(raw.w), bfhi(raw.w)};
; #pragma unroll
;                 for (int e = 0; e < 8; ++e) xc[e] += ct[(32 * kk + 8 * q + e) * 8 + j] * xv[e]; }
;             xb[kk].x = pk2(xc[0], xc[1]); xb[kk].y = pk2(xc[2], xc[3]); xb[kk].z = pk2(xc[4], xc[5]); xb[kk].w = pk2(xc[6], xc[7]);
	v_mov_b32_e32 v116, 0
	v_or_b32_e32 v154, s0, v153
	s_mov_b32 s29, 16
	v_mov_b32_e32 v117, v116
	v_mov_b32_e32 v118, v116
	v_mov_b32_e32 v119, v116
	v_mov_b32_e32 v120, v116
	v_mov_b32_e32 v121, v116
	v_mov_b32_e32 v122, v116
	v_mov_b32_e32 v123, v116
	v_mov_b32_e32 v128, v116
	v_mov_b32_e32 v129, v116
	v_mov_b32_e32 v134, v116
	v_mov_b32_e32 v135, v116
	v_mov_b32_e32 v138, v116
	v_mov_b32_e32 v139, v116
	s_waitcnt vmcnt(4)
	v_mbcnt_lo_u32_b32 v20, -1, 0
	v_mbcnt_hi_u32_b32 v20, -1, v20
	v_and_b32_e32 v20, 1, v20
	v_mul_u32_u24_e32 v20, 28, v20
	v_sub_u32_e32 v20, v151, v20
	ds_write2_b32 v20, v4, v5 offset1:2
	ds_write2_b32 v20, v6, v7 offset0:8 offset1:10
	s_waitcnt vmcnt(0)
	v_mul_f32_e32 v9, 0xbfb8aa3b, v9
	v_mul_f32_e32 v10, 0xbfb8aa3b, v10
	ds_write_b128 v151, v[8:11] offset:16
	s_waitcnt lgkmcnt(0)
	global_load_dwordx4 v[74:77], v[14:15], off
	global_load_dwordx4 v[58:61], v[14:15], off offset:64
	global_load_dwordx4 v[70:73], v[16:17], off
	global_load_dwordx4 v[54:57], v[16:17], off offset:64
	global_load_dwordx4 v[66:69], v[18:19], off
	global_load_dwordx4 v[50:53], v[18:19], off offset:64
	global_load_dwordx4 v[62:65], v[12:13], off
	global_load_dwordx4 v[46:49], v[12:13], off offset:64
	v_mov_b32_e32 v4, 1.0
	v_mov_b32_e32 v5, v4
	v_mov_b32_e32 v8, v4
	v_mov_b32_e32 v9, v4
	v_mov_b32_e32 v12, v4
	v_mov_b32_e32 v13, v4
	v_mov_b32_e32 v6, v116
	v_mov_b32_e32 v7, v116
	v_mov_b32_e32 v136, v4
	v_mov_b32_e32 v137, v4
	v_mov_b32_e32 v132, v4
	v_mov_b32_e32 v133, v4
	v_mov_b32_e32 v130, v4
	v_mov_b32_e32 v131, v4
	v_mov_b32_e32 v126, v4
	v_mov_b32_e32 v127, v4
	s_waitcnt lgkmcnt(4)
	v_mov_b32_e32 v124, v4
	s_waitcnt lgkmcnt(3)
	v_mov_b32_e32 v125, v4
.LBB0_178:
	s_add_i32 s4, s11, s29
	s_cmpk_lg_i32 s29, 0x100
	s_cselect_b32 s0, s29, 0xf0
	v_add_u32_e32 v26, s0, v152
	v_add_u32_e32 v155, s29, v153
	v_max_i32_e32 v10, 0, v26
	v_max_i32_e32 v18, -1, v26
	v_max_i32_e32 v22, -2, v26
	v_max_i32_e32 v26, -3, v26
	v_add_u32_e32 v164, -16, v155
	v_add_u32_e32 v18, 1, v18
	v_add_u32_e32 v22, 2, v22
	v_add_u32_e32 v26, 3, v26
	s_cmp_eq_u32 s4, 16
	v_mad_u64_u32 v[10:11], s[0:1], v10, s88, v[2:3]
	v_mad_u64_u32 v[34:35], s[0:1], v18, s88, v[2:3]
	v_mad_u64_u32 v[38:39], s[0:1], v22, s88, v[2:3]
	v_mad_u64_u32 v[42:43], s[0:1], v26, s88, v[2:3]
	s_cselect_b64 s[20:21], -1, 0
	v_cmp_gt_u32_e64 s[4:5], 3, v164
	s_and_b64 s[0:1], s[20:21], s[4:5]
	v_cmp_gt_u32_e64 s[4:5], 2, v164
	global_load_dwordx4 v[14:17], v[10:11], off
	global_load_dwordx4 v[18:21], v[34:35], off
	global_load_dwordx4 v[22:25], v[38:39], off
	global_load_dwordx4 v[26:29], v[42:43], off
	global_load_dwordx4 v[30:33], v[10:11], off offset:64
	s_nop 0
	global_load_dwordx4 v[34:37], v[34:35], off offset:64
	s_nop 0
	global_load_dwordx4 v[38:41], v[38:39], off offset:64
	s_nop 0
	global_load_dwordx4 v[42:45], v[42:43], off offset:64
	ds_read_b128 v[78:81], v150
	ds_read2_b32 v[160:161], v150 offset0:4 offset1:12
	ds_read_b128 v[156:159], v150 offset:32
	ds_read2_b32 v[162:163], v150 offset0:20 offset1:28
	ds_read2_b32 v[140:141], v150 offset0:36 offset1:44
	ds_read2_b32 v[10:11], v150 offset0:52 offset1:60
	s_and_b64 s[14:15], s[20:21], s[4:5]
	v_cmp_eq_u32_e64 s[4:5], 16, v155
	s_waitcnt vmcnt(15)
	v_cndmask_b32_e64 v74, v74, 0, s[0:1]
	s_and_b64 s[4:5], s[20:21], s[4:5]
	s_waitcnt vmcnt(13)
	v_cndmask_b32_e64 v168, v71, 0, s[14:15]
	v_cndmask_b32_e64 v70, v70, 0, s[14:15]
	s_waitcnt vmcnt(11)
	v_cndmask_b32_e64 v155, v69, 0, s[4:5]
	v_cndmask_b32_e64 v169, v68, 0, s[4:5]
	v_cndmask_b32_e64 v170, v67, 0, s[4:5]
	v_cndmask_b32_e64 v71, v66, 0, s[4:5]
	v_lshlrev_b32_e32 v66, 16, v74
	v_and_b32_e32 v67, 0xffff0000, v74
	s_waitcnt lgkmcnt(5)
	s_waitcnt lgkmcnt(3)
	v_pk_fma_f32 v[66:67], v[78:79], v[66:67], v[160:161]
	v_lshlrev_b32_e32 v68, 16, v70
	v_and_b32_e32 v69, 0xffff0000, v70
	v_pk_fma_f32 v[66:67], v[80:81], v[68:69], v[66:67]
	v_lshlrev_b32_e32 v68, 16, v71
	v_and_b32_e32 v69, 0xffff0000, v71
	v_cndmask_b32_e64 v75, v75, 0, s[0:1]
	v_pk_fma_f32 v[66:67], v[156:157], v[68:69], v[66:67]
	s_waitcnt vmcnt(9)
	v_lshlrev_b32_e32 v68, 16, v62
	v_and_b32_e32 v69, 0xffff0000, v62
	v_cndmask_b32_e64 v165, v77, 0, s[0:1]
	v_cndmask_b32_e64 v166, v76, 0, s[0:1]
	v_cndmask_b32_e64 v164, v73, 0, s[14:15]
	v_cndmask_b32_e64 v167, v72, 0, s[14:15]
	v_pk_fma_f32 v[66:67], v[158:159], v[68:69], v[66:67]
	v_lshlrev_b32_e32 v76, 16, v75
	v_and_b32_e32 v77, 0xffff0000, v75
	ds_read_b128 v[68:71], v150 offset:64
	ds_read_b128 v[72:75], v150 offset:96
	v_lshlrev_b32_e32 v62, 16, v63
	v_and_b32_e32 v63, 0xffff0000, v63
	v_cvt_pk_bf16_f32 v66, v66, v67
	s_waitcnt lgkmcnt(1)
	s_waitcnt lgkmcnt(0)
	v_pk_fma_f32 v[76:77], v[68:69], v[76:77], v[162:163]
	v_lshlrev_b32_e32 v78, 16, v168
	v_and_b32_e32 v79, 0xffff0000, v168
	v_pk_fma_f32 v[68:69], v[70:71], v[78:79], v[76:77]
	v_lshlrev_b32_e32 v76, 16, v170
	v_and_b32_e32 v77, 0xffff0000, v170
	v_pk_fma_f32 v[68:69], v[72:73], v[76:77], v[68:69]
	v_pk_fma_f32 v[62:63], v[74:75], v[62:63], v[68:69]
	ds_read_b128 v[68:71], v150 offset:128
	ds_read_b128 v[72:75], v150 offset:160
	v_lshlrev_b32_e32 v76, 16, v166
	v_and_b32_e32 v77, 0xffff0000, v166
	v_cvt_pk_bf16_f32 v67, v62, v63
	s_waitcnt lgkmcnt(1)
	s_waitcnt lgkmcnt(0)
	v_pk_fma_f32 v[76:77], v[68:69], v[76:77], v[140:141]
	v_lshlrev_b32_e32 v78, 16, v167
	v_and_b32_e32 v79, 0xffff0000, v167
	v_pk_fma_f32 v[68:69], v[70:71], v[78:79], v[76:77]
	v_lshlrev_b32_e32 v76, 16, v169
	v_and_b32_e32 v77, 0xffff0000, v169
	v_pk_fma_f32 v[68:69], v[72:73], v[76:77], v[68:69]
	v_lshlrev_b32_e32 v72, 16, v64
	v_and_b32_e32 v73, 0xffff0000, v64
	v_pk_fma_f32 v[76:77], v[74:75], v[72:73], v[68:69]
	ds_read_b128 v[68:71], v150 offset:192
	ds_read_b128 v[72:75], v150 offset:224
	v_lshlrev_b32_e32 v78, 16, v165
	v_and_b32_e32 v79, 0xffff0000, v165
	v_lshlrev_b32_e32 v64, 16, v65
	s_waitcnt lgkmcnt(1)
; #define LAS __attribute__((address_space(3)))
; __device__ __forceinline__ unsigned pk2(float lo, float hi) { const pk2_f32x2 v = {lo, hi}; return __builtin_bit_cast(unsigned, __builtin_convertvector(v, pk2_bf16x2)); }
; __device__ __forceinline__ void rec1_unit(KArgs args, int L, int unit, LAS unsigned char* lds, int wave, int lane) {
;     ...
;             for (int e = 0; e < 8; ++e) xc[e] = ct[(32 * kk + 8 * q + e) * 8 + 4];
; #pragma unroll
;             for (int j = 0; j < 4; ++j) { const int tt = t - 3 + j;
;                 u32x4 raw = rawc[kk][j];
;                 if (edge && tt < 0) raw = (u32x4){0u, 0u, 0u, 0u};
;                 const float xv[8] = {bflo(raw.x), bfhi(raw.x), bflo(raw.y), bfhi(raw.y), bflo(raw.z), bfhi(raw.z), bflo(raw.w), bfhi(raw.w)};
; #pragma unroll
;                 for (int e = 0; e < 8; ++e) xc[e] += ct[(32 * kk + 8 * q + e) * 8 + j] * xv[e]; }
;             xb[kk].x = pk2(xc[0], xc[1]); xb[kk].y = pk2(xc[2], xc[3]); xb[kk].z = pk2(xc[4], xc[5]); xb[kk].w = pk2(xc[6], xc[7]);
;     ...
;         for (int kh = 0; kh < 2; ++kh) {
;             f32x4 racc[2], iacc[2];
; #pragma unroll
;             for (int nn = 0; nn < 2; ++nn) { racc[nn] = (f32x4){0.f, 0.f, 0.f, 0.f}; iacc[nn] = (f32x4){0.f, 0.f, 0.f, 0.f};
; #pragma unroll
;                 for (int kk = 0; kk < 2; ++kk) { const int n = 2 * kh + nn;
;                     const bf16x8 fa = *(const LAS bf16x8*)(wl + ((0 * 4 + n) * 2 + kk) * 1024 + lane * 16), fx = *(const LAS bf16x8*)(wl + ((1 * 4 + n) * 2 + kk) * 1024 + lane * 16);
;                     const bf16x8 xk = __builtin_bit_cast(bf16x8, xb[kk]);
;                     racc[nn] = __builtin_amdgcn_mfma_f32_16x16x32_bf16(fa, xk, racc[nn], 0, 0, 0); iacc[nn] = __builtin_amdgcn_mfma_f32_16x16x32_bf16(fx, xk, iacc[nn], 0, 0, 0); } }
;             const unsigned xw[4] = {xb[kh].x, xb[kh].y, xb[kh].z, xb[kh].w};
;             float hv[8], av[8];
; #pragma unroll
;             for (int e = 0; e < 8; ++e) {
;                 const int nn = e >> 2, jj = e & 3; const int cb = (32 * kh + 8 * q + e) * 8;
;                 const float xcv = (e & 1) ? bfhi(xw[e >> 1]) : bflo(xw[e >> 1]);
;                 const float r = fsigmoid(racc[nn][jj] + ct[cb + 5]), ig = fsigmoid(iacc[nn][jj] + ct[cb + 6]);
;                 float a = __builtin_amdgcn_exp2f(ct[cb + 7] * r);
	s_waitcnt lgkmcnt(0)
	v_pk_fma_f32 v[10:11], v[68:69], v[78:79], v[10:11]
	v_lshlrev_b32_e32 v78, 16, v164
	v_and_b32_e32 v79, 0xffff0000, v164
	v_pk_fma_f32 v[10:11], v[70:71], v[78:79], v[10:11]
	v_lshlrev_b32_e32 v68, 16, v155
	v_and_b32_e32 v69, 0xffff0000, v155
	v_pk_fma_f32 v[10:11], v[72:73], v[68:69], v[10:11]
	v_and_b32_e32 v65, 0xffff0000, v65
	v_pk_fma_f32 v[10:11], v[74:75], v[64:65], v[10:11]
	v_cvt_pk_bf16_f32 v68, v76, v77
	v_cvt_pk_bf16_f32 v69, v10, v11
	v_add_u32_e32 v10, 0x400, v150
	ds_read2_b32 v[64:65], v10 offset0:4 offset1:12
	ds_read2_b32 v[70:71], v10 offset0:20 offset1:28
	ds_read2_b32 v[62:63], v10 offset0:36 offset1:44
	ds_read2_b32 v[10:11], v10 offset0:52 offset1:60
	v_cndmask_b32_e64 v75, v57, 0, s[14:15]
	v_cndmask_b32_e64 v76, v56, 0, s[14:15]
	v_cndmask_b32_e64 v77, v55, 0, s[14:15]
	v_cndmask_b32_e64 v78, v54, 0, s[14:15]
	v_cndmask_b32_e64 v79, v53, 0, s[4:5]
	v_cndmask_b32_e64 v80, v52, 0, s[4:5]
	v_cndmask_b32_e64 v81, v51, 0, s[4:5]
	v_cndmask_b32_e64 v140, v50, 0, s[4:5]
	ds_read_b128 v[50:53], v150 offset:1024
	ds_read_b128 v[54:57], v150 offset:1056
	v_cndmask_b32_e64 v74, v59, 0, s[0:1]
	v_cndmask_b32_e64 v59, v58, 0, s[0:1]
	v_cndmask_b32_e64 v72, v61, 0, s[0:1]
	v_cndmask_b32_e64 v73, v60, 0, s[0:1]
	v_lshlrev_b32_e32 v58, 16, v59
	v_and_b32_e32 v59, 0xffff0000, v59
	s_waitcnt lgkmcnt(1)
	s_waitcnt lgkmcnt(0)
	v_pk_fma_f32 v[58:59], v[50:51], v[58:59], v[64:65]
	v_lshlrev_b32_e32 v60, 16, v78
	v_and_b32_e32 v61, 0xffff0000, v78
	v_pk_fma_f32 v[50:51], v[52:53], v[60:61], v[58:59]
	v_lshlrev_b32_e32 v58, 16, v140
	v_and_b32_e32 v59, 0xffff0000, v140
	v_pk_fma_f32 v[50:51], v[54:55], v[58:59], v[50:51]
	s_waitcnt vmcnt(8)
	v_lshlrev_b32_e32 v54, 16, v46
	v_and_b32_e32 v55, 0xffff0000, v46
	v_pk_fma_f32 v[50:51], v[56:57], v[54:55], v[50:51]
	ds_read_b128 v[52:55], v150 offset:1088
	ds_read_b128 v[56:59], v150 offset:1120
	v_lshlrev_b32_e32 v60, 16, v74
	v_and_b32_e32 v61, 0xffff0000, v74
	v_lshlrev_b32_e32 v46, 16, v47
	s_waitcnt lgkmcnt(1)
	s_waitcnt lgkmcnt(0)
	v_pk_fma_f32 v[60:61], v[52:53], v[60:61], v[70:71]
	v_lshlrev_b32_e32 v64, 16, v77
	v_and_b32_e32 v65, 0xffff0000, v77
	v_pk_fma_f32 v[52:53], v[54:55], v[64:65], v[60:61]
	v_lshlrev_b32_e32 v60, 16, v81
	v_and_b32_e32 v61, 0xffff0000, v81
	v_pk_fma_f32 v[52:53], v[56:57], v[60:61], v[52:53]
	v_and_b32_e32 v47, 0xffff0000, v47
	v_pk_fma_f32 v[60:61], v[58:59], v[46:47], v[52:53]
	ds_read_b128 v[52:55], v150 offset:1152
	ds_read_b128 v[56:59], v150 offset:1184
	v_lshlrev_b32_e32 v46, 16, v73
	v_and_b32_e32 v47, 0xffff0000, v73
	s_waitcnt lgkmcnt(1)
	s_waitcnt lgkmcnt(0)
	v_pk_fma_f32 v[46:47], v[52:53], v[46:47], v[62:63]
	v_lshlrev_b32_e32 v62, 16, v76
	v_and_b32_e32 v63, 0xffff0000, v76
	v_pk_fma_f32 v[46:47], v[54:55], v[62:63], v[46:47]
	v_lshlrev_b32_e32 v52, 16, v80
	v_and_b32_e32 v53, 0xffff0000, v80
	v_pk_fma_f32 v[46:47], v[56:57], v[52:53], v[46:47]
	v_lshlrev_b32_e32 v52, 16, v48
	v_and_b32_e32 v53, 0xffff0000, v48
	v_pk_fma_f32 v[62:63], v[58:59], v[52:53], v[46:47]
	ds_read_b128 v[52:55], v150 offset:1216
	ds_read_b128 v[56:59], v150 offset:1248
	v_lshlrev_b32_e32 v46, 16, v72
	v_and_b32_e32 v47, 0xffff0000, v72
	s_waitcnt lgkmcnt(1)
	s_waitcnt lgkmcnt(0)
	v_pk_fma_f32 v[10:11], v[52:53], v[46:47], v[10:11]
	v_lshlrev_b32_e32 v46, 16, v75
	v_and_b32_e32 v47, 0xffff0000, v75
	v_pk_fma_f32 v[10:11], v[54:55], v[46:47], v[10:11]
	v_lshlrev_b32_e32 v46, 16, v79
	v_and_b32_e32 v47, 0xffff0000, v79
	v_pk_fma_f32 v[10:11], v[56:57], v[46:47], v[10:11]
	v_lshlrev_b32_e32 v46, 16, v49
	v_and_b32_e32 v47, 0xffff0000, v49
	v_pk_fma_f32 v[10:11], v[58:59], v[46:47], v[10:11]
	v_cvt_pk_bf16_f32 v46, v50, v51
	ds_read_b128 v[50:53], v146
	ds_read_b128 v[54:57], v146 offset:8192
	v_cvt_pk_bf16_f32 v47, v60, v61
	v_cvt_pk_bf16_f32 v48, v62, v63
	ds_read_b128 v[58:61], v146 offset:1024
	ds_read_b128 v[62:65], v146 offset:9216
	s_waitcnt lgkmcnt(3)
	v_mfma_f32_16x16x32_bf16 v[50:53], v[50:53], v[66:69], 0
	v_cvt_pk_bf16_f32 v49, v10, v11
	v_add3_u32 v10, v154, s29, -16
	v_ashrrev_i32_e32 v11, 31, v10
	s_waitcnt lgkmcnt(2)
	v_mfma_f32_16x16x32_bf16 v[54:57], v[54:57], v[66:69], 0
	v_lshlrev_b64 v[10:11], 9, v[10:11]
	v_lshl_add_u64 v[10:11], v[10:11], 0, v[82:83]
	v_lshlrev_b64 v[10:11], 1, v[10:11]
	s_waitcnt lgkmcnt(1)
	v_mfma_f32_16x16x32_bf16 v[50:53], v[58:61], v[46:49], v[50:53]
	s_add_i32 s29, s29, 16
	s_cmpk_eq_i32 s29, 0x110
	s_waitcnt lgkmcnt(0)
	v_mfma_f32_16x16x32_bf16 v[54:57], v[62:65], v[46:49], v[54:57]
	ds_read_b128 v[58:61], v146 offset:2048
	ds_read_b128 v[62:65], v146 offset:10240
	ds_read_b128 v[70:73], v146 offset:3072
	ds_read_b128 v[74:77], v146 offset:11264
	s_waitcnt lgkmcnt(3)
	v_mfma_f32_16x16x32_bf16 v[58:61], v[58:61], v[66:69], 0
	s_waitcnt lgkmcnt(1)
	v_mfma_f32_16x16x32_bf16 v[58:61], v[70:73], v[46:49], v[58:61]
	ds_read2_b32 v[70:71], v150 offset0:5 offset1:6
	v_lshlrev_b32_e32 v72, 16, v66
	s_waitcnt lgkmcnt(0)
	v_fmamk_f32 v50, v50, 0xbfb8aa3b, v70
	s_nop 0
	v_exp_f32_e32 v50, v50
	ds_read_b32 v70, v150 offset:28
	v_fmamk_f32 v54, v54, 0xbfb8aa3b, v71
	s_nop 0
	v_add_f32_e32 v50, 1.0, v50
	v_rcp_f32_e32 v50, v50
	v_exp_f32_e32 v54, v54
	v_mfma_f32_16x16x32_bf16 v[62:65], v[62:65], v[66:69], 0
	s_waitcnt lgkmcnt(0)
; __device__ __forceinline__ float fsigmoid(float x) { return __builtin_amdgcn_rcpf(1.f + __builtin_amdgcn_exp2f(-x * LOG2E)); }
; #define REC_SCAN_STEP(N_) asm volatile("s_nop 1\n\tv_fmac_f32_dpp %0, %0, %1 row_shr:" #N_ " row_mask:0xf bank_mask:0xf\n\ts_nop 1\n\tv_mul_f32_dpp %1, %1, %1 row_shr:" #N_ " row_mask:0xf bank_mask:0xf" : "+v"(bb), "+v"(a))
; __device__ __forceinline__ void rec1_unit(KArgs args, int L, int unit, LAS unsigned char* lds, int wave, int lane) {
;     ...
;             for (int e = 0; e < 8; ++e) {
;                 const int nn = e >> 2, jj = e & 3; const int cb = (32 * kh + 8 * q + e) * 8;
;                 const float xcv = (e & 1) ? bfhi(xw[e >> 1]) : bflo(xw[e >> 1]);
;                 const float r = fsigmoid(racc[nn][jj] + ct[cb + 5]), ig = fsigmoid(iacc[nn][jj] + ct[cb + 6]);
;                 float a = __builtin_amdgcn_exp2f(ct[cb + 7] * r);
;                 float bb = __builtin_amdgcn_sqrtf(fmaxf(1.f - a * a, 0.f)) * (ig * xcv);
;     ...
;                 REC_SCAN_STEP(1); REC_SCAN_STEP(2); REC_SCAN_STEP(4); REC_SCAN_STEP(8);
;     ...
;                 const float hl = a * Hcar[kh][e] + bb, ca = a * Acar[kh][e];
;                 hv[e] = hl; av[e] = ca;
;                 Hcar[kh][e] = __builtin_bit_cast(float, __builtin_amdgcn_ds_bpermute(bidx15, __builtin_bit_cast(int, hl))); Acar[kh][e] = __builtin_bit_cast(float, __builtin_amdgcn_ds_bpermute(bidx15, __builtin_bit_cast(int, ca)));
	v_mul_f32_e32 v50, v70, v50
	v_exp_f32_e32 v71, v50
	v_add_f32_e32 v54, 1.0, v54
	v_rcp_f32_e32 v54, v54
	v_mfma_f32_16x16x32_bf16 v[62:65], v[74:77], v[46:49], v[62:65]
	v_fma_f32 v50, -v71, v71, 1.0
	v_max_f32_e32 v50, 0, v50
	v_sqrt_f32_e32 v50, v50
	v_mul_f32_e32 v54, v54, v72
	v_mul_f32_e32 v73, v54, v50
	s_nop 1
	v_fmac_f32_dpp v73, v73, v71 row_shr:1 row_mask:0xf bank_mask:0xf
	s_nop 1
	v_mul_f32_dpp v71, v71, v71 row_shr:1 row_mask:0xf bank_mask:0xf
	v_and_b32_e32 v50, 0xffff0000, v66
	s_nop 1
	v_fmac_f32_dpp v73, v73, v71 row_shr:2 row_mask:0xf bank_mask:0xf
	s_nop 1
	v_mul_f32_dpp v71, v71, v71 row_shr:2 row_mask:0xf bank_mask:0xf
	s_nop 0
	s_nop 1
	v_fmac_f32_dpp v73, v73, v71 row_shr:4 row_mask:0xf bank_mask:0xf
	s_nop 1
	v_mul_f32_dpp v71, v71, v71 row_shr:4 row_mask:0xf bank_mask:0xf
	s_nop 0
	s_nop 1
	v_fmac_f32_dpp v73, v73, v71 row_shr:8 row_mask:0xf bank_mask:0xf
	s_nop 1
	v_mul_f32_dpp v71, v71, v71 row_shr:8 row_mask:0xf bank_mask:0xf
	ds_read2_b32 v[74:75], v150 offset0:13 offset1:14
	s_waitcnt lgkmcnt(0)
	v_fmamk_f32 v51, v51, 0xbfb8aa3b, v74
	s_nop 0
	v_exp_f32_e32 v51, v51
	v_fmamk_f32 v54, v55, 0xbfb8aa3b, v75
	ds_read_b32 v55, v150 offset:60
	s_nop 0
	v_add_f32_e32 v51, 1.0, v51
	v_rcp_f32_e32 v51, v51
	v_exp_f32_e32 v54, v54
	s_waitcnt lgkmcnt(0)
	v_mul_f32_e32 v51, v55, v51
	v_exp_f32_e32 v70, v51
	v_add_f32_e32 v54, 1.0, v54
	v_rcp_f32_e32 v54, v54
	v_fma_f32 v51, -v70, v70, 1.0
	v_max_f32_e32 v51, 0, v51
	v_sqrt_f32_e32 v51, v51
	v_mul_f32_e32 v50, v54, v50
	v_mul_f32_e32 v72, v50, v51
	s_nop 1
	v_fmac_f32_dpp v72, v72, v70 row_shr:1 row_mask:0xf bank_mask:0xf
	s_nop 1
	v_mul_f32_dpp v70, v70, v70 row_shr:1 row_mask:0xf bank_mask:0xf
	s_nop 0
	s_nop 1
	v_fmac_f32_dpp v72, v72, v70 row_shr:2 row_mask:0xf bank_mask:0xf
	s_nop 1
	v_mul_f32_dpp v70, v70, v70 row_shr:2 row_mask:0xf bank_mask:0xf
	s_nop 0
	s_nop 1
	v_fmac_f32_dpp v72, v72, v70 row_shr:4 row_mask:0xf bank_mask:0xf
	s_nop 1
	v_mul_f32_dpp v70, v70, v70 row_shr:4 row_mask:0xf bank_mask:0xf
	s_nop 0
	s_nop 1
	v_fmac_f32_dpp v72, v72, v70 row_shr:8 row_mask:0xf bank_mask:0xf
	s_nop 1
	v_mul_f32_dpp v70, v70, v70 row_shr:8 row_mask:0xf bank_mask:0xf
	s_nop 0
	v_pk_fma_f32 v[50:51], v[6:7], v[70:71], v[72:73]
	ds_bpermute_b32 v7, v149, v51
	v_pk_mul_f32 v[54:55], v[12:13], v[70:71]
	v_pk_mov_b32 v[70:71], v[50:51], v[50:51] op_sel:[1,0]
	ds_bpermute_b32 v6, v149, v50
	ds_read2_b32 v[50:51], v150 offset0:21 offset1:22
	v_pk_mov_b32 v[72:73], v[54:55], v[54:55] op_sel:[1,0]
	ds_bpermute_b32 v12, v149, v54
	v_lshlrev_b32_e32 v54, 16, v67
	ds_bpermute_b32 v13, v149, v55
	s_waitcnt lgkmcnt(2)
	v_fmamk_f32 v51, v56, 0xbfb8aa3b, v51
	v_fmamk_f32 v50, v52, 0xbfb8aa3b, v50
	s_nop 0
	s_nop 0
	v_exp_f32_e32 v51, v51
	v_exp_f32_e32 v50, v50
	v_add_f32_e32 v51, 1.0, v51
	v_add_f32_e32 v50, 1.0, v50
	v_rcp_f32_e32 v52, v51
	ds_read_b32 v51, v150 offset:92
	v_rcp_f32_e32 v50, v50
	v_mul_f32_e32 v52, v52, v54
	s_waitcnt lgkmcnt(0)
	v_mul_f32_e32 v50, v51, v50
	v_exp_f32_e32 v51, v50
	s_nop 0
	v_fma_f32 v50, -v51, v51, 1.0
	v_max_f32_e32 v50, 0, v50
	v_sqrt_f32_e32 v50, v50
	s_nop 0
	v_mul_f32_e32 v55, v52, v50
	s_nop 1
	v_fmac_f32_dpp v55, v55, v51 row_shr:1 row_mask:0xf bank_mask:0xf
	s_nop 1
	v_mul_f32_dpp v51, v51, v51 row_shr:1 row_mask:0xf bank_mask:0xf
	v_and_b32_e32 v52, 0xffff0000, v67
	s_nop 1
	v_fmac_f32_dpp v55, v55, v51 row_shr:2 row_mask:0xf bank_mask:0xf
	s_nop 1
	v_mul_f32_dpp v51, v51, v51 row_shr:2 row_mask:0xf bank_mask:0xf
	s_nop 0
	s_nop 1
	v_fmac_f32_dpp v55, v55, v51 row_shr:4 row_mask:0xf bank_mask:0xf
	s_nop 1
	v_mul_f32_dpp v51, v51, v51 row_shr:4 row_mask:0xf bank_mask:0xf
	s_nop 0
	s_nop 1
	v_fmac_f32_dpp v55, v55, v51 row_shr:8 row_mask:0xf bank_mask:0xf
	s_nop 1
	v_mul_f32_dpp v51, v51, v51 row_shr:8 row_mask:0xf bank_mask:0xf
	ds_read2_b32 v[74:75], v150 offset0:29 offset1:30
	ds_read_b32 v54, v150 offset:124
	s_waitcnt lgkmcnt(1)
	v_fmamk_f32 v50, v53, 0xbfb8aa3b, v74
	s_nop 0
	v_exp_f32_e32 v50, v50
	v_fmamk_f32 v53, v57, 0xbfb8aa3b, v75
	s_nop 0
	v_exp_f32_e32 v53, v53
	v_add_f32_e32 v50, 1.0, v50
	v_rcp_f32_e32 v50, v50
	v_add_f32_e32 v53, 1.0, v53
	v_rcp_f32_e32 v53, v53
	s_waitcnt lgkmcnt(0)
	v_mul_f32_e32 v50, v54, v50
	v_exp_f32_e32 v50, v50
	v_mul_f32_e32 v52, v53, v52
	v_fma_f32 v54, -v50, v50, 1.0
	v_max_f32_e32 v54, 0, v54
	v_sqrt_f32_e32 v54, v54
	s_nop 0
	v_mul_f32_e32 v54, v52, v54
	s_nop 1
	v_fmac_f32_dpp v54, v54, v50 row_shr:1 row_mask:0xf bank_mask:0xf
	s_nop 1
	v_mul_f32_dpp v50, v50, v50 row_shr:1 row_mask:0xf bank_mask:0xf
	s_nop 0
	s_nop 1
	v_fmac_f32_dpp v54, v54, v50 row_shr:2 row_mask:0xf bank_mask:0xf
	s_nop 1
	v_mul_f32_dpp v50, v50, v50 row_shr:2 row_mask:0xf bank_mask:0xf
	s_nop 0
	s_nop 1
	v_fmac_f32_dpp v54, v54, v50 row_shr:4 row_mask:0xf bank_mask:0xf
	s_nop 1
	v_mul_f32_dpp v50, v50, v50 row_shr:4 row_mask:0xf bank_mask:0xf
	s_nop 0
	s_nop 1
	v_fmac_f32_dpp v54, v54, v50 row_shr:8 row_mask:0xf bank_mask:0xf
	s_nop 1
	v_mul_f32_dpp v50, v50, v50 row_shr:8 row_mask:0xf bank_mask:0xf
	s_nop 0
	v_pk_fma_f32 v[52:53], v[138:139], v[50:51], v[54:55]
	v_pk_mul_f32 v[50:51], v[8:9], v[50:51]
	ds_bpermute_b32 v9, v149, v51
	v_pk_mov_b32 v[56:57], v[50:51], v[50:51] op_sel:[1,0]
	ds_bpermute_b32 v8, v149, v50
	ds_read2_b32 v[50:51], v150 offset0:37 offset1:38
	ds_bpermute_b32 v139, v149, v53
	v_pk_mov_b32 v[54:55], v[52:53], v[52:53] op_sel:[1,0]
	ds_bpermute_b32 v138, v149, v52
	v_lshlrev_b32_e32 v52, 16, v68
	s_waitcnt lgkmcnt(2)
	v_fmamk_f32 v51, v62, 0xbfb8aa3b, v51
	v_fmamk_f32 v50, v58, 0xbfb8aa3b, v50
	s_nop 0
	s_nop 0
	v_exp_f32_e32 v51, v51
	v_exp_f32_e32 v50, v50
	v_add_f32_e32 v51, 1.0, v51
	v_add_f32_e32 v50, 1.0, v50
	v_rcp_f32_e32 v53, v51
	ds_read_b32 v51, v150 offset:156
	v_rcp_f32_e32 v50, v50
	v_mul_f32_e32 v52, v53, v52
	s_waitcnt lgkmcnt(0)
; __device__ __forceinline__ unsigned pk2(float lo, float hi) { const pk2_f32x2 v = {lo, hi}; return __builtin_bit_cast(unsigned, __builtin_convertvector(v, pk2_bf16x2)); }
; __device__ __forceinline__ float fsigmoid(float x) { return __builtin_amdgcn_rcpf(1.f + __builtin_amdgcn_exp2f(-x * LOG2E)); }
; #define REC_SCAN_STEP(N_) asm volatile("s_nop 1\n\tv_fmac_f32_dpp %0, %0, %1 row_shr:" #N_ " row_mask:0xf bank_mask:0xf\n\ts_nop 1\n\tv_mul_f32_dpp %1, %1, %1 row_shr:" #N_ " row_mask:0xf bank_mask:0xf" : "+v"(bb), "+v"(a))
; __device__ __forceinline__ void rec1_unit(KArgs args, int L, int unit, LAS unsigned char* lds, int wave, int lane) {
;     ...
;             for (int e = 0; e < 8; ++e) {
;                 const int nn = e >> 2, jj = e & 3; const int cb = (32 * kh + 8 * q + e) * 8;
;                 const float xcv = (e & 1) ? bfhi(xw[e >> 1]) : bflo(xw[e >> 1]);
;                 const float r = fsigmoid(racc[nn][jj] + ct[cb + 5]), ig = fsigmoid(iacc[nn][jj] + ct[cb + 6]);
;                 float a = __builtin_amdgcn_exp2f(ct[cb + 7] * r);
;                 float bb = __builtin_amdgcn_sqrtf(fmaxf(1.f - a * a, 0.f)) * (ig * xcv);
;     ...
;                 REC_SCAN_STEP(1); REC_SCAN_STEP(2); REC_SCAN_STEP(4); REC_SCAN_STEP(8);
;     ...
;                 const float hl = a * Hcar[kh][e] + bb, ca = a * Acar[kh][e];
;                 hv[e] = hl; av[e] = ca;
;                 Hcar[kh][e] = __builtin_bit_cast(float, __builtin_amdgcn_ds_bpermute(bidx15, __builtin_bit_cast(int, hl))); Acar[kh][e] = __builtin_bit_cast(float, __builtin_amdgcn_ds_bpermute(bidx15, __builtin_bit_cast(int, ca)));
;             }
;             const size_t o = (size_t)(b * SEQ + t) * D_REC + 64 * hb + 32 * kh + 8 * q;
;             u32x4 w; w.x = pk2(hv[0], hv[1]); w.y = pk2(hv[2], hv[3]); w.z = pk2(hv[4], hv[5]); w.w = pk2(hv[6], hv[7]);
;             *(u32x4*)(hloc + o) = w;
;             w.x = pk2(av[0], av[1]); w.y = pk2(av[2], av[3]); w.z = pk2(av[4], av[5]); w.w = pk2(av[6], av[7]);
;             *(u32x4*)(cumA + o) = w;
	v_mul_f32_e32 v50, v51, v50
	v_exp_f32_e32 v51, v50
	s_nop 0
	v_fma_f32 v50, -v51, v51, 1.0
	v_max_f32_e32 v50, 0, v50
	v_sqrt_f32_e32 v50, v50
	s_nop 0
	v_mul_f32_e32 v53, v52, v50
	s_nop 1
	v_fmac_f32_dpp v53, v53, v51 row_shr:1 row_mask:0xf bank_mask:0xf
	s_nop 1
	v_mul_f32_dpp v51, v51, v51 row_shr:1 row_mask:0xf bank_mask:0xf
	v_and_b32_e32 v52, 0xffff0000, v68
	s_nop 1
	v_fmac_f32_dpp v53, v53, v51 row_shr:2 row_mask:0xf bank_mask:0xf
	s_nop 1
	v_mul_f32_dpp v51, v51, v51 row_shr:2 row_mask:0xf bank_mask:0xf
	s_nop 0
	s_nop 1
	v_fmac_f32_dpp v53, v53, v51 row_shr:4 row_mask:0xf bank_mask:0xf
	s_nop 1
	v_mul_f32_dpp v51, v51, v51 row_shr:4 row_mask:0xf bank_mask:0xf
	s_nop 0
	s_nop 1
	v_fmac_f32_dpp v53, v53, v51 row_shr:8 row_mask:0xf bank_mask:0xf
	s_nop 1
	v_mul_f32_dpp v51, v51, v51 row_shr:8 row_mask:0xf bank_mask:0xf
	ds_read2_b32 v[74:75], v150 offset0:45 offset1:46
	s_waitcnt lgkmcnt(0)
	v_fmamk_f32 v50, v59, 0xbfb8aa3b, v74
	s_nop 0
	v_exp_f32_e32 v50, v50
	ds_read_b32 v59, v150 offset:188
	v_fmamk_f32 v58, v63, 0xbfb8aa3b, v75
	s_nop 0
	v_add_f32_e32 v50, 1.0, v50
	v_rcp_f32_e32 v50, v50
	v_exp_f32_e32 v58, v58
	s_waitcnt lgkmcnt(0)
	v_mul_f32_e32 v50, v59, v50
	v_exp_f32_e32 v50, v50
	v_add_f32_e32 v58, 1.0, v58
	v_rcp_f32_e32 v58, v58
	v_fma_f32 v59, -v50, v50, 1.0
	v_max_f32_e32 v59, 0, v59
	v_sqrt_f32_e32 v59, v59
	v_mul_f32_e32 v52, v58, v52
	v_mul_f32_e32 v52, v52, v59
	s_nop 1
	v_fmac_f32_dpp v52, v52, v50 row_shr:1 row_mask:0xf bank_mask:0xf
	s_nop 1
	v_mul_f32_dpp v50, v50, v50 row_shr:1 row_mask:0xf bank_mask:0xf
	s_nop 0
	s_nop 1
	v_fmac_f32_dpp v52, v52, v50 row_shr:2 row_mask:0xf bank_mask:0xf
	s_nop 1
	v_mul_f32_dpp v50, v50, v50 row_shr:2 row_mask:0xf bank_mask:0xf
	s_nop 0
	s_nop 1
	v_fmac_f32_dpp v52, v52, v50 row_shr:4 row_mask:0xf bank_mask:0xf
	s_nop 1
	v_mul_f32_dpp v50, v50, v50 row_shr:4 row_mask:0xf bank_mask:0xf
	s_nop 0
	s_nop 1
	v_fmac_f32_dpp v52, v52, v50 row_shr:8 row_mask:0xf bank_mask:0xf
	s_nop 1
	v_mul_f32_dpp v50, v50, v50 row_shr:8 row_mask:0xf bank_mask:0xf
	s_nop 0
	v_pk_fma_f32 v[52:53], v[134:135], v[50:51], v[52:53]
	v_pk_mul_f32 v[50:51], v[4:5], v[50:51]
	ds_bpermute_b32 v5, v149, v51
	v_pk_mov_b32 v[62:63], v[50:51], v[50:51] op_sel:[1,0]
	ds_bpermute_b32 v4, v149, v50
	ds_read2_b32 v[50:51], v150 offset0:53 offset1:54
	ds_bpermute_b32 v135, v149, v53
	v_pk_mov_b32 v[58:59], v[52:53], v[52:53] op_sel:[1,0]
	ds_bpermute_b32 v134, v149, v52
	v_lshlrev_b32_e32 v52, 16, v69
	s_waitcnt lgkmcnt(2)
	v_fmamk_f32 v51, v64, 0xbfb8aa3b, v51
	v_fmamk_f32 v50, v60, 0xbfb8aa3b, v50
	s_nop 0
	s_nop 0
	v_exp_f32_e32 v51, v51
	v_exp_f32_e32 v50, v50
	v_add_f32_e32 v51, 1.0, v51
	v_add_f32_e32 v50, 1.0, v50
	v_rcp_f32_e32 v53, v51
	ds_read_b32 v51, v150 offset:220
	v_rcp_f32_e32 v50, v50
	v_mul_f32_e32 v52, v53, v52
	s_waitcnt lgkmcnt(0)
	v_mul_f32_e32 v50, v51, v50
	v_exp_f32_e32 v51, v50
	s_nop 0
	v_fma_f32 v50, -v51, v51, 1.0
	v_max_f32_e32 v50, 0, v50
	v_sqrt_f32_e32 v50, v50
	s_nop 0
	v_mul_f32_e32 v53, v52, v50
	s_nop 1
	v_fmac_f32_dpp v53, v53, v51 row_shr:1 row_mask:0xf bank_mask:0xf
	s_nop 1
	v_mul_f32_dpp v51, v51, v51 row_shr:1 row_mask:0xf bank_mask:0xf
	v_and_b32_e32 v52, 0xffff0000, v69
	s_nop 1
	v_fmac_f32_dpp v53, v53, v51 row_shr:2 row_mask:0xf bank_mask:0xf
	s_nop 1
	v_mul_f32_dpp v51, v51, v51 row_shr:2 row_mask:0xf bank_mask:0xf
	s_nop 0
	s_nop 1
	v_fmac_f32_dpp v53, v53, v51 row_shr:4 row_mask:0xf bank_mask:0xf
	s_nop 1
	v_mul_f32_dpp v51, v51, v51 row_shr:4 row_mask:0xf bank_mask:0xf
	s_nop 0
	s_nop 1
	v_fmac_f32_dpp v53, v53, v51 row_shr:8 row_mask:0xf bank_mask:0xf
	s_nop 1
	v_mul_f32_dpp v51, v51, v51 row_shr:8 row_mask:0xf bank_mask:0xf
	ds_read2_b32 v[74:75], v150 offset0:61 offset1:62
	s_waitcnt lgkmcnt(0)
	v_fmamk_f32 v50, v61, 0xbfb8aa3b, v74
	s_nop 0
	v_exp_f32_e32 v50, v50
	ds_read_b32 v61, v150 offset:252
	v_fmamk_f32 v60, v65, 0xbfb8aa3b, v75
	s_nop 0
	v_add_f32_e32 v50, 1.0, v50
	v_rcp_f32_e32 v50, v50
	v_exp_f32_e32 v60, v60
	s_waitcnt vmcnt(7)
	v_mov_b64_e32 v[76:77], v[16:17]
	v_mov_b64_e32 v[74:75], v[14:15]
	s_waitcnt lgkmcnt(0)
	v_mul_f32_e32 v50, v61, v50
	v_exp_f32_e32 v50, v50
	v_add_f32_e32 v60, 1.0, v60
	v_rcp_f32_e32 v60, v60
	v_fma_f32 v61, -v50, v50, 1.0
	v_max_f32_e32 v61, 0, v61
	v_sqrt_f32_e32 v61, v61
	v_mul_f32_e32 v52, v60, v52
	v_mov_b32_e32 v60, v51
	v_mul_f32_e32 v52, v52, v61
	s_nop 1
	v_fmac_f32_dpp v52, v52, v50 row_shr:1 row_mask:0xf bank_mask:0xf
	s_nop 1
	v_mul_f32_dpp v50, v50, v50 row_shr:1 row_mask:0xf bank_mask:0xf
	s_nop 0
	s_nop 1
	v_fmac_f32_dpp v52, v52, v50 row_shr:2 row_mask:0xf bank_mask:0xf
	s_nop 1
	v_mul_f32_dpp v50, v50, v50 row_shr:2 row_mask:0xf bank_mask:0xf
	s_nop 0
	s_nop 1
	v_fmac_f32_dpp v52, v52, v50 row_shr:4 row_mask:0xf bank_mask:0xf
	s_nop 1
	v_mul_f32_dpp v50, v50, v50 row_shr:4 row_mask:0xf bank_mask:0xf
	s_nop 0
	s_nop 1
	v_fmac_f32_dpp v52, v52, v50 row_shr:8 row_mask:0xf bank_mask:0xf
	s_nop 1
	v_mul_f32_dpp v50, v50, v50 row_shr:8 row_mask:0xf bank_mask:0xf
	s_nop 0
	v_pk_fma_f32 v[52:53], v[128:129], v[50:51], v[52:53]
	v_mov_b32_e32 v61, v50
	v_pk_mov_b32 v[64:65], v[52:53], v[52:53] op_sel:[1,0]
	ds_bpermute_b32 v129, v149, v53
	v_pk_mul_f32 v[60:61], v[136:137], v[60:61]
	ds_bpermute_b32 v128, v149, v52
	v_cvt_pk_bf16_f32 v50, v70, v71
	v_cvt_pk_bf16_f32 v51, v54, v55
	v_cvt_pk_bf16_f32 v52, v58, v59
	v_cvt_pk_bf16_f32 v53, v64, v65
	v_lshl_add_u64 v[54:55], s[6:7], 0, v[10:11]
	global_store_dwordx4 v[54:55], v[50:53], off
	v_lshl_add_u64 v[54:55], s[18:19], 0, v[10:11]
	ds_bpermute_b32 v136, v149, v60
	v_cvt_pk_bf16_f32 v50, v72, v73
	v_cvt_pk_bf16_f32 v51, v56, v57
	v_cvt_pk_bf16_f32 v52, v62, v63
	v_cvt_pk_bf16_f32 v53, v60, v61
	global_store_dwordx4 v[54:55], v[50:53], off
	ds_read_b128 v[50:53], v146 offset:4096
	ds_read_b128 v[54:57], v146 offset:12288
	ds_bpermute_b32 v137, v149, v61
	ds_read_b128 v[58:61], v146 offset:5120
	ds_read_b128 v[70:73], v146 offset:13312
	s_waitcnt lgkmcnt(4)
; #define LAS __attribute__((address_space(3)))
; __device__ __forceinline__ float fsigmoid(float x) { return __builtin_amdgcn_rcpf(1.f + __builtin_amdgcn_exp2f(-x * LOG2E)); }
; #define REC_SCAN_STEP(N_) asm volatile("s_nop 1\n\tv_fmac_f32_dpp %0, %0, %1 row_shr:" #N_ " row_mask:0xf bank_mask:0xf\n\ts_nop 1\n\tv_mul_f32_dpp %1, %1, %1 row_shr:" #N_ " row_mask:0xf bank_mask:0xf" : "+v"(bb), "+v"(a))
; __device__ __forceinline__ void rec1_unit(KArgs args, int L, int unit, LAS unsigned char* lds, int wave, int lane) {
;     ...
;         for (int kh = 0; kh < 2; ++kh) {
;             f32x4 racc[2], iacc[2];
; #pragma unroll
;             for (int nn = 0; nn < 2; ++nn) { racc[nn] = (f32x4){0.f, 0.f, 0.f, 0.f}; iacc[nn] = (f32x4){0.f, 0.f, 0.f, 0.f};
; #pragma unroll
;                 for (int kk = 0; kk < 2; ++kk) { const int n = 2 * kh + nn;
;                     const bf16x8 fa = *(const LAS bf16x8*)(wl + ((0 * 4 + n) * 2 + kk) * 1024 + lane * 16), fx = *(const LAS bf16x8*)(wl + ((1 * 4 + n) * 2 + kk) * 1024 + lane * 16);
;                     const bf16x8 xk = __builtin_bit_cast(bf16x8, xb[kk]);
;                     racc[nn] = __builtin_amdgcn_mfma_f32_16x16x32_bf16(fa, xk, racc[nn], 0, 0, 0); iacc[nn] = __builtin_amdgcn_mfma_f32_16x16x32_bf16(fx, xk, iacc[nn], 0, 0, 0); } }
;             const unsigned xw[4] = {xb[kh].x, xb[kh].y, xb[kh].z, xb[kh].w};
;             float hv[8], av[8];
; #pragma unroll
;             for (int e = 0; e < 8; ++e) {
;                 const int nn = e >> 2, jj = e & 3; const int cb = (32 * kh + 8 * q + e) * 8;
;                 const float xcv = (e & 1) ? bfhi(xw[e >> 1]) : bflo(xw[e >> 1]);
;                 const float r = fsigmoid(racc[nn][jj] + ct[cb + 5]), ig = fsigmoid(iacc[nn][jj] + ct[cb + 6]);
;                 float a = __builtin_amdgcn_exp2f(ct[cb + 7] * r);
;                 float bb = __builtin_amdgcn_sqrtf(fmaxf(1.f - a * a, 0.f)) * (ig * xcv);
;     ...
;                 REC_SCAN_STEP(1); REC_SCAN_STEP(2); REC_SCAN_STEP(4); REC_SCAN_STEP(8);
;     ...
;                 const float hl = a * Hcar[kh][e] + bb, ca = a * Acar[kh][e];
;                 hv[e] = hl; av[e] = ca;
;                 Hcar[kh][e] = __builtin_bit_cast(float, __builtin_amdgcn_ds_bpermute(bidx15, __builtin_bit_cast(int, hl))); Acar[kh][e] = __builtin_bit_cast(float, __builtin_amdgcn_ds_bpermute(bidx15, __builtin_bit_cast(int, ca)));
	v_mfma_f32_16x16x32_bf16 v[50:53], v[50:53], v[66:69], 0
	v_or_b32_e32 v10, 64, v10
	s_waitcnt lgkmcnt(3)
	v_mfma_f32_16x16x32_bf16 v[54:57], v[54:57], v[66:69], 0
	s_waitcnt lgkmcnt(1)
	v_mfma_f32_16x16x32_bf16 v[62:65], v[58:61], v[46:49], v[50:53]
	s_waitcnt lgkmcnt(0)
	v_mfma_f32_16x16x32_bf16 v[58:61], v[70:73], v[46:49], v[54:57]
	s_nop 0
	ds_read_b128 v[50:53], v146 offset:6144
	s_nop 1
	ds_read_b128 v[54:57], v146 offset:14336
	s_waitcnt lgkmcnt(1)
	v_mfma_f32_16x16x32_bf16 v[50:53], v[50:53], v[66:69], 0
	s_waitcnt lgkmcnt(0)
	v_mfma_f32_16x16x32_bf16 v[66:69], v[54:57], v[66:69], 0
	ds_read_b128 v[54:57], v146 offset:7168
	ds_read_b128 v[70:73], v146 offset:15360
	s_waitcnt lgkmcnt(1)
	v_mfma_f32_16x16x32_bf16 v[54:57], v[54:57], v[46:49], v[50:53]
	s_waitcnt lgkmcnt(0)
	v_mfma_f32_16x16x32_bf16 v[50:53], v[70:73], v[46:49], v[66:69]
	s_nop 2
	v_add_u32_e32 v67, 0x414, v150
	ds_read2_b32 v[68:69], v67 offset1:1
	ds_read_b32 v67, v150 offset:1052
	v_lshlrev_b32_e32 v66, 16, v46
	v_and_b32_e32 v46, 0xffff0000, v46
	s_waitcnt lgkmcnt(1)
	v_fmamk_f32 v62, v62, 0xbfb8aa3b, v68
	s_nop 0
	v_exp_f32_e32 v62, v62
	v_fmamk_f32 v58, v58, 0xbfb8aa3b, v69
	s_nop 0
	v_exp_f32_e32 v58, v58
	v_add_f32_e32 v62, 1.0, v62
	v_rcp_f32_e32 v62, v62
	v_add_f32_e32 v58, 1.0, v58
	v_rcp_f32_e32 v58, v58
	s_waitcnt lgkmcnt(0)
	v_mul_f32_e32 v62, v67, v62
	v_exp_f32_e32 v67, v62
	v_mul_f32_e32 v58, v58, v66
	v_fma_f32 v62, -v67, v67, 1.0
	v_max_f32_e32 v62, 0, v62
	v_sqrt_f32_e32 v62, v62
	s_nop 0
	v_mul_f32_e32 v69, v58, v62
	s_nop 1
	v_fmac_f32_dpp v69, v69, v67 row_shr:1 row_mask:0xf bank_mask:0xf
	s_nop 1
	v_mul_f32_dpp v67, v67, v67 row_shr:1 row_mask:0xf bank_mask:0xf
	v_add_u32_e32 v58, 0x434, v150
	s_nop 1
	v_fmac_f32_dpp v69, v69, v67 row_shr:2 row_mask:0xf bank_mask:0xf
	s_nop 1
	v_mul_f32_dpp v67, v67, v67 row_shr:2 row_mask:0xf bank_mask:0xf
	s_nop 0
	s_nop 1
	v_fmac_f32_dpp v69, v69, v67 row_shr:4 row_mask:0xf bank_mask:0xf
	s_nop 1
	v_mul_f32_dpp v67, v67, v67 row_shr:4 row_mask:0xf bank_mask:0xf
	s_nop 0
	s_nop 1
	v_fmac_f32_dpp v69, v69, v67 row_shr:8 row_mask:0xf bank_mask:0xf
	s_nop 1
	v_mul_f32_dpp v67, v67, v67 row_shr:8 row_mask:0xf bank_mask:0xf
	ds_read2_b32 v[70:71], v58 offset1:1
	ds_read_b32 v62, v150 offset:1084
	s_waitcnt lgkmcnt(1)
	v_fmamk_f32 v58, v63, 0xbfb8aa3b, v70
	s_nop 0
	v_exp_f32_e32 v58, v58
	v_fmamk_f32 v59, v59, 0xbfb8aa3b, v71
	s_nop 0
	v_exp_f32_e32 v59, v59
	v_add_f32_e32 v58, 1.0, v58
	v_rcp_f32_e32 v58, v58
	s_waitcnt vmcnt(8)
	v_mov_b64_e32 v[72:73], v[20:21]
	v_add_f32_e32 v59, 1.0, v59
	v_rcp_f32_e32 v59, v59
	s_waitcnt lgkmcnt(0)
	v_mul_f32_e32 v58, v62, v58
	v_exp_f32_e32 v66, v58
	v_mov_b64_e32 v[70:71], v[18:19]
	v_mul_f32_e32 v46, v59, v46
	v_fma_f32 v58, -v66, v66, 1.0
	v_max_f32_e32 v58, 0, v58
	v_sqrt_f32_e32 v58, v58
	s_nop 0
	v_mul_f32_e32 v68, v46, v58
	s_nop 1
	v_fmac_f32_dpp v68, v68, v66 row_shr:1 row_mask:0xf bank_mask:0xf
	s_nop 1
	v_mul_f32_dpp v66, v66, v66 row_shr:1 row_mask:0xf bank_mask:0xf
	v_mov_b32_e32 v58, v67
	s_nop 1
	v_fmac_f32_dpp v68, v68, v66 row_shr:2 row_mask:0xf bank_mask:0xf
	s_nop 1
	v_mul_f32_dpp v66, v66, v66 row_shr:2 row_mask:0xf bank_mask:0xf
	v_lshlrev_b32_e32 v46, 16, v47
	s_nop 1
	v_fmac_f32_dpp v68, v68, v66 row_shr:4 row_mask:0xf bank_mask:0xf
	s_nop 1
	v_mul_f32_dpp v66, v66, v66 row_shr:4 row_mask:0xf bank_mask:0xf
	s_nop 0
	s_nop 1
	v_fmac_f32_dpp v68, v68, v66 row_shr:8 row_mask:0xf bank_mask:0xf
	s_nop 1
	v_mul_f32_dpp v66, v66, v66 row_shr:8 row_mask:0xf bank_mask:0xf
	s_nop 0
	v_pk_fma_f32 v[68:69], v[122:123], v[66:67], v[68:69]
	v_mov_b32_e32 v59, v66
	v_add_u32_e32 v66, 0x454, v150
	ds_read2_b32 v[66:67], v66 offset1:1
	ds_bpermute_b32 v123, v149, v69
	v_pk_mov_b32 v[62:63], v[68:69], v[68:69] op_sel:[1,0]
	ds_bpermute_b32 v122, v149, v68
	v_pk_mul_f32 v[58:59], v[132:133], v[58:59]
	s_waitcnt lgkmcnt(2)
	v_fmamk_f32 v64, v64, 0xbfb8aa3b, v66
	s_nop 0
	v_exp_f32_e32 v64, v64
	ds_read_b32 v66, v150 offset:1116
	v_fmamk_f32 v60, v60, 0xbfb8aa3b, v67
	s_nop 0
	v_add_f32_e32 v64, 1.0, v64
	v_rcp_f32_e32 v64, v64
	v_exp_f32_e32 v60, v60
	ds_bpermute_b32 v132, v149, v58
	ds_bpermute_b32 v133, v149, v59
	s_waitcnt lgkmcnt(2)
	v_mul_f32_e32 v64, v66, v64
	v_exp_f32_e32 v67, v64
	v_add_f32_e32 v60, 1.0, v60
	v_rcp_f32_e32 v60, v60
	v_fma_f32 v64, -v67, v67, 1.0
	v_max_f32_e32 v64, 0, v64
	v_sqrt_f32_e32 v64, v64
	v_mul_f32_e32 v46, v60, v46
	v_and_b32_e32 v60, 0xffff0000, v47
	v_mul_f32_e32 v69, v46, v64
	s_nop 1
	v_fmac_f32_dpp v69, v69, v67 row_shr:1 row_mask:0xf bank_mask:0xf
	s_nop 1
	v_mul_f32_dpp v67, v67, v67 row_shr:1 row_mask:0xf bank_mask:0xf
	v_add_u32_e32 v46, 0x474, v150
	s_nop 1
	v_fmac_f32_dpp v69, v69, v67 row_shr:2 row_mask:0xf bank_mask:0xf
	s_nop 1
	v_mul_f32_dpp v67, v67, v67 row_shr:2 row_mask:0xf bank_mask:0xf
	s_nop 0
	s_nop 1
	v_fmac_f32_dpp v69, v69, v67 row_shr:4 row_mask:0xf bank_mask:0xf
	s_nop 1
	v_mul_f32_dpp v67, v67, v67 row_shr:4 row_mask:0xf bank_mask:0xf
	s_nop 0
	s_nop 1
	v_fmac_f32_dpp v69, v69, v67 row_shr:8 row_mask:0xf bank_mask:0xf
	s_nop 1
	v_mul_f32_dpp v67, v67, v67 row_shr:8 row_mask:0xf bank_mask:0xf
	ds_read2_b32 v[46:47], v46 offset1:1
	s_waitcnt lgkmcnt(0)
	v_fmamk_f32 v46, v65, 0xbfb8aa3b, v46
	s_nop 0
	v_exp_f32_e32 v46, v46
	v_fmamk_f32 v47, v61, 0xbfb8aa3b, v47
	ds_read_b32 v61, v150 offset:1148
	s_nop 0
	v_add_f32_e32 v46, 1.0, v46
	v_rcp_f32_e32 v46, v46
	v_exp_f32_e32 v47, v47
	s_waitcnt lgkmcnt(0)
; __device__ __forceinline__ float fsigmoid(float x) { return __builtin_amdgcn_rcpf(1.f + __builtin_amdgcn_exp2f(-x * LOG2E)); }
; #define REC_SCAN_STEP(N_) asm volatile("s_nop 1\n\tv_fmac_f32_dpp %0, %0, %1 row_shr:" #N_ " row_mask:0xf bank_mask:0xf\n\ts_nop 1\n\tv_mul_f32_dpp %1, %1, %1 row_shr:" #N_ " row_mask:0xf bank_mask:0xf" : "+v"(bb), "+v"(a))
; __device__ __forceinline__ void rec1_unit(KArgs args, int L, int unit, LAS unsigned char* lds, int wave, int lane) {
;     ...
;             for (int e = 0; e < 8; ++e) {
;                 const int nn = e >> 2, jj = e & 3; const int cb = (32 * kh + 8 * q + e) * 8;
;                 const float xcv = (e & 1) ? bfhi(xw[e >> 1]) : bflo(xw[e >> 1]);
;                 const float r = fsigmoid(racc[nn][jj] + ct[cb + 5]), ig = fsigmoid(iacc[nn][jj] + ct[cb + 6]);
;                 float a = __builtin_amdgcn_exp2f(ct[cb + 7] * r);
;                 float bb = __builtin_amdgcn_sqrtf(fmaxf(1.f - a * a, 0.f)) * (ig * xcv);
;     ...
;                 REC_SCAN_STEP(1); REC_SCAN_STEP(2); REC_SCAN_STEP(4); REC_SCAN_STEP(8);
;     ...
;                 const float hl = a * Hcar[kh][e] + bb, ca = a * Acar[kh][e];
;                 hv[e] = hl; av[e] = ca;
;                 Hcar[kh][e] = __builtin_bit_cast(float, __builtin_amdgcn_ds_bpermute(bidx15, __builtin_bit_cast(int, hl))); Acar[kh][e] = __builtin_bit_cast(float, __builtin_amdgcn_ds_bpermute(bidx15, __builtin_bit_cast(int, ca)));
	v_mul_f32_e32 v46, v61, v46
	v_exp_f32_e32 v66, v46
	v_add_f32_e32 v47, 1.0, v47
	v_rcp_f32_e32 v47, v47
	v_fma_f32 v46, -v66, v66, 1.0
	v_max_f32_e32 v46, 0, v46
	v_sqrt_f32_e32 v46, v46
	v_mul_f32_e32 v47, v47, v60
	v_mul_f32_e32 v68, v47, v46
	s_nop 1
	v_fmac_f32_dpp v68, v68, v66 row_shr:1 row_mask:0xf bank_mask:0xf
	s_nop 1
	v_mul_f32_dpp v66, v66, v66 row_shr:1 row_mask:0xf bank_mask:0xf
	v_mov_b32_e32 v46, v67
	s_nop 1
	v_fmac_f32_dpp v68, v68, v66 row_shr:2 row_mask:0xf bank_mask:0xf
	s_nop 1
	v_mul_f32_dpp v66, v66, v66 row_shr:2 row_mask:0xf bank_mask:0xf
	s_nop 0
	s_nop 1
	v_fmac_f32_dpp v68, v68, v66 row_shr:4 row_mask:0xf bank_mask:0xf
	s_nop 1
	v_mul_f32_dpp v66, v66, v66 row_shr:4 row_mask:0xf bank_mask:0xf
	s_nop 0
	s_nop 1
	v_fmac_f32_dpp v68, v68, v66 row_shr:8 row_mask:0xf bank_mask:0xf
	s_nop 1
	v_mul_f32_dpp v66, v66, v66 row_shr:8 row_mask:0xf bank_mask:0xf
	s_nop 0
	v_pk_fma_f32 v[64:65], v[120:121], v[66:67], v[68:69]
	ds_bpermute_b32 v120, v149, v64
	v_pk_mov_b32 v[60:61], v[64:65], v[64:65] op_sel:[1,0]
	v_add_u32_e32 v64, 0x494, v150
	ds_bpermute_b32 v121, v149, v65
	ds_read2_b32 v[64:65], v64 offset1:1
	v_mov_b32_e32 v47, v66
	v_lshlrev_b32_e32 v66, 16, v48
	v_and_b32_e32 v48, 0xffff0000, v48
	v_pk_mul_f32 v[46:47], v[130:131], v[46:47]
	s_waitcnt lgkmcnt(0)
	v_fmamk_f32 v54, v54, 0xbfb8aa3b, v64
	s_nop 0
	v_exp_f32_e32 v54, v54
	ds_read_b32 v64, v150 offset:1180
	v_fmamk_f32 v50, v50, 0xbfb8aa3b, v65
	s_nop 0
	v_add_f32_e32 v54, 1.0, v54
	v_rcp_f32_e32 v54, v54
	v_exp_f32_e32 v50, v50
	ds_bpermute_b32 v130, v149, v46
	ds_bpermute_b32 v131, v149, v47
	s_waitcnt lgkmcnt(2)
	v_mul_f32_e32 v54, v64, v54
	v_exp_f32_e32 v65, v54
	v_add_f32_e32 v50, 1.0, v50
	v_rcp_f32_e32 v50, v50
	v_fma_f32 v54, -v65, v65, 1.0
	v_max_f32_e32 v54, 0, v54
	v_sqrt_f32_e32 v54, v54
	v_mul_f32_e32 v50, v50, v66
	v_mul_f32_e32 v67, v50, v54
	s_nop 1
	v_fmac_f32_dpp v67, v67, v65 row_shr:1 row_mask:0xf bank_mask:0xf
	s_nop 1
	v_mul_f32_dpp v65, v65, v65 row_shr:1 row_mask:0xf bank_mask:0xf
	v_add_u32_e32 v50, 0x4b4, v150
	s_nop 1
	v_fmac_f32_dpp v67, v67, v65 row_shr:2 row_mask:0xf bank_mask:0xf
	s_nop 1
	v_mul_f32_dpp v65, v65, v65 row_shr:2 row_mask:0xf bank_mask:0xf
	s_nop 0
	s_nop 1
	v_fmac_f32_dpp v67, v67, v65 row_shr:4 row_mask:0xf bank_mask:0xf
	s_nop 1
	v_mul_f32_dpp v65, v65, v65 row_shr:4 row_mask:0xf bank_mask:0xf
	s_nop 0
	s_nop 1
	v_fmac_f32_dpp v67, v67, v65 row_shr:8 row_mask:0xf bank_mask:0xf
	s_nop 1
	v_mul_f32_dpp v65, v65, v65 row_shr:8 row_mask:0xf bank_mask:0xf
	ds_read2_b32 v[68:69], v50 offset1:1
	ds_read_b32 v54, v150 offset:1212
	s_waitcnt lgkmcnt(1)
	v_fmamk_f32 v50, v55, 0xbfb8aa3b, v68
	s_nop 0
	v_exp_f32_e32 v50, v50
	v_fmamk_f32 v51, v51, 0xbfb8aa3b, v69
	s_nop 0
	v_exp_f32_e32 v51, v51
	v_add_f32_e32 v50, 1.0, v50
	v_rcp_f32_e32 v50, v50
	v_add_f32_e32 v51, 1.0, v51
	v_rcp_f32_e32 v51, v51
	s_waitcnt lgkmcnt(0)
	v_mul_f32_e32 v50, v54, v50
	v_exp_f32_e32 v64, v50
	v_mul_f32_e32 v48, v51, v48
	v_fma_f32 v50, -v64, v64, 1.0
	v_max_f32_e32 v50, 0, v50
	v_sqrt_f32_e32 v50, v50
	s_nop 0
	v_mul_f32_e32 v66, v48, v50
	s_nop 1
	v_fmac_f32_dpp v66, v66, v64 row_shr:1 row_mask:0xf bank_mask:0xf
	s_nop 1
	v_mul_f32_dpp v64, v64, v64 row_shr:1 row_mask:0xf bank_mask:0xf
	v_mov_b32_e32 v50, v65
	s_nop 1
	v_fmac_f32_dpp v66, v66, v64 row_shr:2 row_mask:0xf bank_mask:0xf
	s_nop 1
	v_mul_f32_dpp v64, v64, v64 row_shr:2 row_mask:0xf bank_mask:0xf
	v_lshlrev_b32_e32 v48, 16, v49
	s_nop 1
	v_fmac_f32_dpp v66, v66, v64 row_shr:4 row_mask:0xf bank_mask:0xf
	s_nop 1
	v_mul_f32_dpp v64, v64, v64 row_shr:4 row_mask:0xf bank_mask:0xf
	s_nop 0
	s_nop 1
	v_fmac_f32_dpp v66, v66, v64 row_shr:8 row_mask:0xf bank_mask:0xf
	s_nop 1
	v_mul_f32_dpp v64, v64, v64 row_shr:8 row_mask:0xf bank_mask:0xf
	s_nop 0
	v_pk_fma_f32 v[66:67], v[118:119], v[64:65], v[66:67]
	v_mov_b32_e32 v51, v64
	v_add_u32_e32 v64, 0x4d4, v150
	ds_read2_b32 v[64:65], v64 offset1:1
	ds_bpermute_b32 v119, v149, v67
	v_pk_mov_b32 v[54:55], v[66:67], v[66:67] op_sel:[1,0]
	ds_bpermute_b32 v118, v149, v66
	v_pk_mul_f32 v[50:51], v[126:127], v[50:51]
	s_waitcnt lgkmcnt(2)
	v_fmamk_f32 v56, v56, 0xbfb8aa3b, v64
	s_nop 0
	v_exp_f32_e32 v56, v56
	ds_read_b32 v64, v150 offset:1244
	v_fmamk_f32 v52, v52, 0xbfb8aa3b, v65
	s_nop 0
	v_add_f32_e32 v56, 1.0, v56
	v_rcp_f32_e32 v56, v56
	v_exp_f32_e32 v52, v52
	v_cvt_pk_bf16_f32 v54, v54, v55
	ds_bpermute_b32 v126, v149, v50
	s_waitcnt lgkmcnt(1)
; __device__ __forceinline__ unsigned pk2(float lo, float hi) { const pk2_f32x2 v = {lo, hi}; return __builtin_bit_cast(unsigned, __builtin_convertvector(v, pk2_bf16x2)); }
; __device__ __forceinline__ float fsigmoid(float x) { return __builtin_amdgcn_rcpf(1.f + __builtin_amdgcn_exp2f(-x * LOG2E)); }
; __device__ __forceinline__ void rec1_unit(KArgs args, int L, int unit, LAS unsigned char* lds, int wave, int lane) {
;     ...
;             for (int e = 0; e < 8; ++e) {
;                 const int nn = e >> 2, jj = e & 3; const int cb = (32 * kh + 8 * q + e) * 8;
;                 const float xcv = (e & 1) ? bfhi(xw[e >> 1]) : bflo(xw[e >> 1]);
;                 const float r = fsigmoid(racc[nn][jj] + ct[cb + 5]), ig = fsigmoid(iacc[nn][jj] + ct[cb + 6]);
;                 float a = __builtin_amdgcn_exp2f(ct[cb + 7] * r);
;                 float bb = __builtin_amdgcn_sqrtf(fmaxf(1.f - a * a, 0.f)) * (ig * xcv);
;     ...
;                 REC_SCAN_STEP(1); REC_SCAN_STEP(2); REC_SCAN_STEP(4); REC_SCAN_STEP(8);
;     ...
;                 const float hl = a * Hcar[kh][e] + bb, ca = a * Acar[kh][e];
;                 hv[e] = hl; av[e] = ca;
;                 Hcar[kh][e] = __builtin_bit_cast(float, __builtin_amdgcn_ds_bpermute(bidx15, __builtin_bit_cast(int, hl))); Acar[kh][e] = __builtin_bit_cast(float, __builtin_amdgcn_ds_bpermute(bidx15, __builtin_bit_cast(int, ca)));
;             }
;             const size_t o = (size_t)(b * SEQ + t) * D_REC + 64 * hb + 32 * kh + 8 * q;
;             u32x4 w; w.x = pk2(hv[0], hv[1]); w.y = pk2(hv[2], hv[3]); w.z = pk2(hv[4], hv[5]); w.w = pk2(hv[6], hv[7]);
;             *(u32x4*)(hloc + o) = w;
;             w.x = pk2(av[0], av[1]); w.y = pk2(av[2], av[3]); w.z = pk2(av[4], av[5]); w.w = pk2(av[6], av[7]);
;             *(u32x4*)(cumA + o) = w;
;             asm volatile("" ::: "memory");
;         }
; #pragma unroll
;         for (int kk = 0; kk < 2; ++kk)
; #pragma unroll
;             for (int j = 0; j < 4; ++j) rawc[kk][j] = rawn[kk][j];
;     }
;     ...
;     if (fr == 0) {
; #pragma unroll
;         for (int kk = 0; kk < 2; ++kk)
; #pragma unroll
;             for (int e = 0; e < 8; ++e) { const int c = 64 * hb + 32 * kk + 8 * q + e; float* ap = agg + ((size_t)(b * 16 + chk) * 512 + c) * 2; ap[0] = Acar[kk][e]; ap[1] = Hcar[kk][e]; }
	v_mul_f32_e32 v56, v64, v56
	v_exp_f32_e32 v65, v56
	v_add_f32_e32 v52, 1.0, v52
	v_rcp_f32_e32 v52, v52
	ds_bpermute_b32 v127, v149, v51
	v_fma_f32 v56, -v65, v65, 1.0
	v_max_f32_e32 v56, 0, v56
	v_sqrt_f32_e32 v56, v56
	v_mul_f32_e32 v48, v52, v48
	v_and_b32_e32 v52, 0xffff0000, v49
	v_cvt_pk_bf16_f32 v50, v50, v51
	v_mul_f32_e32 v67, v48, v56
	s_nop 1
	v_fmac_f32_dpp v67, v67, v65 row_shr:1 row_mask:0xf bank_mask:0xf
	s_nop 1
	v_mul_f32_dpp v65, v65, v65 row_shr:1 row_mask:0xf bank_mask:0xf
	v_add_u32_e32 v48, 0x4f4, v150
	s_nop 1
	v_fmac_f32_dpp v67, v67, v65 row_shr:2 row_mask:0xf bank_mask:0xf
	s_nop 1
	v_mul_f32_dpp v65, v65, v65 row_shr:2 row_mask:0xf bank_mask:0xf
	s_nop 0
	s_nop 1
	v_fmac_f32_dpp v67, v67, v65 row_shr:4 row_mask:0xf bank_mask:0xf
	s_nop 1
	v_mul_f32_dpp v65, v65, v65 row_shr:4 row_mask:0xf bank_mask:0xf
	s_nop 0
	s_nop 1
	v_fmac_f32_dpp v67, v67, v65 row_shr:8 row_mask:0xf bank_mask:0xf
	s_nop 1
	v_mul_f32_dpp v65, v65, v65 row_shr:8 row_mask:0xf bank_mask:0xf
	ds_read2_b32 v[48:49], v48 offset1:1
	s_waitcnt lgkmcnt(0)
	v_fmamk_f32 v48, v57, 0xbfb8aa3b, v48
	s_nop 0
	v_exp_f32_e32 v48, v48
	v_fmamk_f32 v49, v53, 0xbfb8aa3b, v49
	ds_read_b32 v53, v150 offset:1276
	s_nop 0
	v_add_f32_e32 v48, 1.0, v48
	v_rcp_f32_e32 v48, v48
	v_exp_f32_e32 v49, v49
	s_waitcnt lgkmcnt(0)
	v_mul_f32_e32 v48, v53, v48
	v_exp_f32_e32 v64, v48
	v_add_f32_e32 v49, 1.0, v49
	v_rcp_f32_e32 v49, v49
	v_fma_f32 v48, -v64, v64, 1.0
	v_max_f32_e32 v48, 0, v48
	v_sqrt_f32_e32 v48, v48
	v_mul_f32_e32 v49, v49, v52
	v_mov_b32_e32 v52, v65
	v_mul_f32_e32 v66, v49, v48
	s_nop 1
	v_fmac_f32_dpp v66, v66, v64 row_shr:1 row_mask:0xf bank_mask:0xf
	s_nop 1
	v_mul_f32_dpp v64, v64, v64 row_shr:1 row_mask:0xf bank_mask:0xf
	s_nop 0
	s_nop 1
	v_fmac_f32_dpp v66, v66, v64 row_shr:2 row_mask:0xf bank_mask:0xf
	s_nop 1
	v_mul_f32_dpp v64, v64, v64 row_shr:2 row_mask:0xf bank_mask:0xf
	s_nop 0
	s_nop 1
	v_fmac_f32_dpp v66, v66, v64 row_shr:4 row_mask:0xf bank_mask:0xf
	s_nop 1
	v_mul_f32_dpp v64, v64, v64 row_shr:4 row_mask:0xf bank_mask:0xf
	s_nop 0
	s_nop 1
	v_fmac_f32_dpp v66, v66, v64 row_shr:8 row_mask:0xf bank_mask:0xf
	s_nop 1
	v_mul_f32_dpp v64, v64, v64 row_shr:8 row_mask:0xf bank_mask:0xf
	s_nop 0
	v_pk_fma_f32 v[48:49], v[116:117], v[64:65], v[66:67]
	v_mov_b32_e32 v53, v64
	v_pk_mov_b32 v[64:65], v[48:49], v[48:49] op_sel:[1,0]
	ds_bpermute_b32 v117, v149, v49
	v_pk_mul_f32 v[56:57], v[124:125], v[52:53]
	ds_bpermute_b32 v116, v149, v48
	v_cvt_pk_bf16_f32 v52, v62, v63
	v_cvt_pk_bf16_f32 v53, v60, v61
	v_cvt_pk_bf16_f32 v55, v64, v65
	v_lshl_add_u64 v[48:49], s[6:7], 0, v[10:11]
	ds_bpermute_b32 v124, v149, v56
	ds_bpermute_b32 v125, v149, v57
	global_store_dwordx4 v[48:49], v[52:55], off
	v_cvt_pk_bf16_f32 v48, v58, v59
	v_cvt_pk_bf16_f32 v49, v46, v47
	v_cvt_pk_bf16_f32 v51, v56, v57
	v_lshl_add_u64 v[10:11], s[18:19], 0, v[10:11]
	global_store_dwordx4 v[10:11], v[48:51], off
	s_waitcnt vmcnt(5)
	v_mov_b64_e32 v[52:53], v[40:41]
	v_mov_b64_e32 v[56:57], v[36:37]
	s_waitcnt vmcnt(4)
	v_mov_b64_e32 v[48:49], v[44:45]
	v_mov_b64_e32 v[60:61], v[32:33]
	v_mov_b64_e32 v[64:65], v[28:29]
	v_mov_b64_e32 v[68:69], v[24:25]
	v_mov_b64_e32 v[46:47], v[42:43]
	v_mov_b64_e32 v[50:51], v[38:39]
	v_mov_b64_e32 v[54:55], v[34:35]
	v_mov_b64_e32 v[58:59], v[30:31]
	v_mov_b64_e32 v[62:63], v[26:27]
	v_mov_b64_e32 v[66:67], v[22:23]
	s_cbranch_scc0 .LBB0_178
	s_and_saveexec_b64 s[0:1], vcc
	s_cbranch_execz .LBB0_174
	s_ashr_i32 s11, s10, 31
	s_lshl_b64 s[4:5], s[10:11], 12
	s_add_u32 s4, s23, s4
	s_addc_u32 s5, s25, s5
	v_lshl_add_u64 v[2:3], s[4:5], 0, v[84:85]
	v_mov_b32_e32 v10, v13
	v_mov_b32_e32 v11, v7
	v_mov_b32_e32 v13, v6
	global_store_dwordx4 v[2:3], v[10:13], off
	v_lshl_add_u64 v[2:3], s[4:5], 0, v[86:87]
	v_mov_b32_e32 v6, v9
	v_mov_b32_e32 v7, v139
	v_mov_b32_e32 v9, v138
	global_store_dwordx4 v[2:3], v[6:9], off
	v_mov_b32_e32 v2, v5
	v_mov_b32_e32 v3, v135
	v_lshl_add_u64 v[6:7], s[4:5], 0, v[88:89]
	v_mov_b32_e32 v5, v134
	global_store_dwordx4 v[6:7], v[2:5], off
	v_lshl_add_u64 v[6:7], s[4:5], 0, v[90:91]
	s_nop 0
	v_mov_b32_e32 v2, v136
	v_mov_b32_e32 v3, v129
	v_mov_b32_e32 v4, v137
	v_mov_b32_e32 v5, v128
	global_store_dwordx4 v[6:7], v[2:5], off
	v_lshl_add_u64 v[6:7], s[4:5], 0, v[92:93]
	s_nop 0
	v_mov_b32_e32 v2, v132
	v_mov_b32_e32 v3, v123
	v_mov_b32_e32 v4, v133
	v_mov_b32_e32 v5, v122
	global_store_dwordx4 v[6:7], v[2:5], off
	v_lshl_add_u64 v[6:7], s[4:5], 0, v[94:95]
	s_nop 0
	v_mov_b32_e32 v2, v130
	v_mov_b32_e32 v3, v121
	v_mov_b32_e32 v4, v131
	v_mov_b32_e32 v5, v120
	global_store_dwordx4 v[6:7], v[2:5], off
	v_lshl_add_u64 v[6:7], s[4:5], 0, v[96:97]
	s_nop 0
	v_mov_b32_e32 v2, v126
	v_mov_b32_e32 v3, v119
	v_mov_b32_e32 v4, v127
	v_mov_b32_e32 v5, v118
	global_store_dwordx4 v[6:7], v[2:5], off
	v_lshl_add_u64 v[6:7], s[4:5], 0, v[98:99]
	s_waitcnt lgkmcnt(1)
	v_mov_b32_e32 v2, v124
	v_mov_b32_e32 v3, v117
	s_waitcnt lgkmcnt(0)
	v_mov_b32_e32 v4, v125
	v_mov_b32_e32 v5, v116
	global_store_dwordx4 v[6:7], v[2:5], off
	s_branch .LBB0_174
